# baseline (speedup 1.0000x reference)
.Lmy_ffn_noprio:
	s_mov_b32 s18, s6
	s_lshl_b32 s6, s6, 13
	s_cmp_lg_u32 0, -1
	s_cselect_b32 s7, 0, 0
	s_add_i32 s10, s7, s6
	s_mov_b64 s[6:7], 0x2000
	s_add_i32 s8, s10, 0x13400
	v_lshl_add_u64 v[24:25], v[180:181], 0, s[6:7]
	s_mov_b32 s9, m0
	s_mov_b32 m0, s8
	s_nop 0
	global_load_lds_dwordx4 v[24:25], off
	s_mov_b32 m0, s9
	s_mov_b64 s[8:9], 0xa000
	v_lshl_add_u64 v[24:25], v[180:181], 0, s[8:9]
	s_add_i32 s8, s10, 0x13800
	s_mov_b32 s9, m0
	s_mov_b32 m0, s8
	s_nop 0
	global_load_lds_dwordx4 v[24:25], off
	s_mov_b32 m0, s9
	s_mov_b64 s[8:9], 0x2400
	s_add_i32 s11, s10, 0x13c00
	v_lshl_add_u64 v[24:25], v[180:181], 0, s[8:9]
	s_mov_b32 s8, m0
	s_mov_b32 m0, s11
	s_nop 0
	global_load_lds_dwordx4 v[24:25], off
	s_mov_b32 m0, s8
	s_mov_b64 s[8:9], 0xa400
	v_lshl_add_u64 v[24:25], v[180:181], 0, s[8:9]
	s_add_i32 s8, s10, 0x14000
	s_mov_b32 s9, m0
	s_mov_b32 m0, s8
	s_nop 0
	global_load_lds_dwordx4 v[24:25], off
	s_mov_b32 m0, s9
	s_mov_b64 s[8:9], 0x2800
	s_add_i32 s11, s10, 0x14400
	v_lshl_add_u64 v[24:25], v[180:181], 0, s[8:9]
	s_mov_b32 s8, m0
	s_mov_b32 m0, s11
	s_nop 0
	global_load_lds_dwordx4 v[24:25], off
	s_mov_b32 m0, s8
	s_mov_b64 s[8:9], 0xa800
	v_lshl_add_u64 v[24:25], v[180:181], 0, s[8:9]
	s_add_i32 s8, s10, 0x14800
	s_mov_b32 s9, m0
	s_mov_b32 m0, s8
	s_nop 0
	global_load_lds_dwordx4 v[24:25], off
	s_mov_b32 m0, s9
	s_mov_b64 s[8:9], 0x2c00
	s_add_i32 s11, s10, 0x14c00
	v_lshl_add_u64 v[24:25], v[180:181], 0, s[8:9]
	s_mov_b32 s8, m0
	s_mov_b32 m0, s11
	s_nop 0
	global_load_lds_dwordx4 v[24:25], off
	s_mov_b32 m0, s8
	s_mov_b64 s[8:9], 0xac00
	v_lshl_add_u64 v[24:25], v[180:181], 0, s[8:9]
	s_add_i32 s9, 0, 0x11400
	v_lshl_add_u32 v19, v37, 2, s9
	s_add_i32 s10, s10, 0x15000
	s_mov_b32 s8, m0
	s_mov_b32 m0, s10
	s_nop 0
	global_load_lds_dwordx4 v[24:25], off
	s_mov_b32 m0, s8
	s_waitcnt vmcnt(8)
	ds_write_b128 v19, v[20:23]
	v_lshrrev_b32_e32 v19, 5, v0
	v_mul_u32_u24_e32 v19, 0x410, v19
	v_and_b32_e32 v18, 0x1f0, v18
	v_add3_u32 v19, 0, v19, v18
	ds_write_b128 v19, v[14:17] offset:512
	v_lshrrev_b32_e32 v14, 5, v186
	v_mul_u32_u24_e32 v14, 0x410, v14
	v_add3_u32 v14, 0, v14, v18
	ds_write_b128 v14, v[6:9] offset:512
	v_lshrrev_b32_e32 v6, 5, v182
	v_mul_u32_u24_e32 v6, 0x410, v6
	v_add3_u32 v6, 0, v6, v18
	s_movk_i32 s10, 0x410
	ds_write_b128 v6, v[2:5] offset:512
	v_lshrrev_b32_e32 v2, 5, v185
	v_mul_u32_u24_e32 v2, 0x410, v2
	v_mad_u32_u24 v189, v205, s10, 0
	v_add3_u32 v2, 0, v2, v18
	v_lshl_add_u32 v202, v208, 4, v189
	ds_write_b128 v2, v[10:13] offset:512
	s_waitcnt lgkmcnt(0)
	s_barrier
	ds_read_b128 v[2:5], v202 offset:512
	ds_read_b128 v[102:105], v202 offset:544
	ds_read_b128 v[6:9], v202 offset:33792
	ds_read_b128 v[106:109], v202 offset:33824
	v_mul_u32_u24_e32 v187, 0x410, v205
	global_load_dwordx4 v[110:113], v[128:129], off
	s_waitcnt vmcnt(8) lgkmcnt(3)
	v_mfma_f32_32x32x16_f16 v[18:33], v[38:41], v[2:5], 0
	ds_read_b128 v[114:117], v202 offset:576
	ds_read_b128 v[118:121], v202 offset:33856
	s_waitcnt lgkmcnt(3)
	v_mfma_f32_32x32x16_f16 v[2:17], v[38:41], v[6:9], 0
	global_load_dwordx4 v[38:41], v[128:129], off offset:1024
	s_waitcnt vmcnt(8)
	v_mfma_f32_32x32x16_f16 v[18:33], v[42:45], v[102:105], v[18:33]
	ds_read_b128 v[102:105], v202 offset:608
	ds_read_b128 v[122:125], v202 offset:33888
	s_waitcnt lgkmcnt(4)
	v_mfma_f32_32x32x16_f16 v[2:17], v[42:45], v[106:109], v[2:17]
	global_load_dwordx4 v[42:45], v[128:129], off offset:2048
	s_waitcnt vmcnt(8) lgkmcnt(3)
	v_mfma_f32_32x32x16_f16 v[18:33], v[46:49], v[114:117], v[18:33]
	ds_read_b128 v[106:109], v202 offset:640
	ds_read_b128 v[114:117], v202 offset:33920
	s_waitcnt lgkmcnt(4)
	v_mfma_f32_32x32x16_f16 v[2:17], v[46:49], v[118:121], v[2:17]
	global_load_dwordx4 v[46:49], v[128:129], off offset:3072
	s_waitcnt vmcnt(8) lgkmcnt(3)
	v_mfma_f32_32x32x16_f16 v[18:33], v[50:53], v[102:105], v[18:33]
	ds_read_b128 v[102:105], v202 offset:672
	ds_read_b128 v[118:121], v202 offset:33952
	s_waitcnt lgkmcnt(4)
	v_mfma_f32_32x32x16_f16 v[2:17], v[50:53], v[122:125], v[2:17]
	s_movk_i32 s8, 0x3000
	v_add_co_u32_e32 v126, vcc, s8, v126
	s_waitcnt vmcnt(7) lgkmcnt(3)
	v_mfma_f32_32x32x16_f16 v[18:33], v[54:57], v[106:109], v[18:33]
	v_addc_co_u32_e32 v127, vcc, 0, v127, vcc
	global_load_dwordx4 v[50:53], v[126:127], off
	ds_read_b128 v[106:109], v202 offset:704
	ds_read_b128 v[122:125], v202 offset:33984
	s_waitcnt lgkmcnt(4)
	v_mfma_f32_32x32x16_f16 v[2:17], v[54:57], v[114:117], v[2:17]
	global_load_dwordx4 v[54:57], v[126:127], off offset:1024
	s_waitcnt vmcnt(8) lgkmcnt(3)
	v_mfma_f32_32x32x16_f16 v[18:33], v[58:61], v[102:105], v[18:33]
	ds_read_b128 v[102:105], v202 offset:736
	ds_read_b128 v[114:117], v202 offset:34016
	s_waitcnt lgkmcnt(4)
	v_mfma_f32_32x32x16_f16 v[2:17], v[58:61], v[118:121], v[2:17]
	global_load_dwordx4 v[58:61], v[126:127], off offset:2048
	s_waitcnt vmcnt(8) lgkmcnt(3)
	v_mfma_f32_32x32x16_f16 v[18:33], v[62:65], v[106:109], v[18:33]
	ds_read_b128 v[106:109], v202 offset:768
	ds_read_b128 v[118:121], v202 offset:34048
	s_waitcnt lgkmcnt(4)
	v_mfma_f32_32x32x16_f16 v[2:17], v[62:65], v[122:125], v[2:17]
	global_load_dwordx4 v[62:65], v[126:127], off offset:3072
	s_waitcnt vmcnt(8) lgkmcnt(3)
	v_mfma_f32_32x32x16_f16 v[18:33], v[98:101], v[102:105], v[18:33]
	ds_read_b128 v[102:105], v202 offset:800
	ds_read_b128 v[122:125], v202 offset:34080
	s_waitcnt lgkmcnt(4)
	v_mfma_f32_32x32x16_f16 v[2:17], v[98:101], v[114:117], v[2:17]
	s_waitcnt vmcnt(7) lgkmcnt(3)
	v_mfma_f32_32x32x16_f16 v[18:33], v[110:113], v[106:109], v[18:33]
	ds_read_b128 v[98:101], v202 offset:832
	ds_read_b128 v[106:109], v202 offset:34112
	s_waitcnt lgkmcnt(4)
	v_mfma_f32_32x32x16_f16 v[2:17], v[110:113], v[118:121], v[2:17]
	s_waitcnt vmcnt(6) lgkmcnt(3)
	v_mfma_f32_32x32x16_f16 v[18:33], v[38:41], v[102:105], v[18:33]
	ds_read_b128 v[102:105], v202 offset:864
	ds_read_b128 v[110:113], v202 offset:34144
	s_waitcnt lgkmcnt(4)
	v_mfma_f32_32x32x16_f16 v[2:17], v[38:41], v[122:125], v[2:17]
	s_waitcnt vmcnt(5) lgkmcnt(3)
	v_mfma_f32_32x32x16_f16 v[18:33], v[42:45], v[98:101], v[18:33]
	ds_read_b128 v[38:41], v202 offset:896
	ds_read_b128 v[98:101], v202 offset:34176
	s_waitcnt lgkmcnt(4)
	v_mfma_f32_32x32x16_f16 v[2:17], v[42:45], v[106:109], v[2:17]
	s_waitcnt vmcnt(4) lgkmcnt(3)
	v_mfma_f32_32x32x16_f16 v[18:33], v[46:49], v[102:105], v[18:33]
	ds_read_b128 v[42:45], v202 offset:928
	ds_read_b128 v[102:105], v202 offset:34208
	s_waitcnt lgkmcnt(4)
	v_mfma_f32_32x32x16_f16 v[2:17], v[46:49], v[110:113], v[2:17]
	s_waitcnt vmcnt(3) lgkmcnt(3)
	v_mfma_f32_32x32x16_f16 v[18:33], v[50:53], v[38:41], v[18:33]
	ds_read_b128 v[38:41], v202 offset:960
	ds_read_b128 v[46:49], v202 offset:34240
	s_waitcnt lgkmcnt(4)
	v_mfma_f32_32x32x16_f16 v[2:17], v[50:53], v[98:101], v[2:17]
	s_waitcnt vmcnt(2) lgkmcnt(3)
	v_mfma_f32_32x32x16_f16 v[18:33], v[54:57], v[42:45], v[18:33]
	ds_read_b128 v[42:45], v202 offset:992
	ds_read_b128 v[50:53], v202 offset:34272
	s_waitcnt lgkmcnt(4)
	v_mfma_f32_32x32x16_f16 v[2:17], v[54:57], v[102:105], v[2:17]
	s_waitcnt vmcnt(1) lgkmcnt(3)
	v_mfma_f32_32x32x16_f16 v[18:33], v[58:61], v[38:41], v[18:33]
	s_waitcnt lgkmcnt(2)
	v_mfma_f32_32x32x16_f16 v[2:17], v[58:61], v[46:49], v[2:17]
	s_waitcnt vmcnt(0) lgkmcnt(1)
	v_mfma_f32_32x32x16_f16 v[18:33], v[62:65], v[42:45], v[18:33]
	s_waitcnt lgkmcnt(0)
	v_mfma_f32_32x32x16_f16 v[2:17], v[62:65], v[50:53], v[2:17]
	v_and_b32_e32 v188, 0xfc, v37
	v_lshl_add_u32 v35, v188, 1, 0
	v_cvt_pk_f16_f32 v39, v92, v93
	v_cvt_pk_f16_f32 v38, v90, v91
	v_mad_u32_u24 v37, v209, s10, v35
	ds_write_b64 v37, v[38:39]
	v_lshrrev_b32_e32 v37, 6, v186
	v_cvt_pk_f16_f32 v39, v96, v97
	v_cvt_pk_f16_f32 v38, v94, v95
	v_mad_u32_u24 v40, v37, s10, v35
	v_lshrrev_b32_e32 v44, 6, v182
	ds_write_b64 v40, v[38:39]
	v_cvt_pk_f16_f32 v39, v88, v89
	v_cvt_pk_f16_f32 v38, v86, v87
	v_mad_u32_u24 v40, v44, s10, v35
	v_lshrrev_b32_e32 v45, 6, v185
	ds_write_b64 v40, v[38:39]
	v_cvt_pk_f16_f32 v39, v84, v85
	v_cvt_pk_f16_f32 v38, v82, v83
	v_mad_u32_u24 v40, v45, s10, v35
	v_lshrrev_b32_e32 v46, 6, v179
	ds_write_b64 v40, v[38:39]
	v_cvt_pk_f16_f32 v39, v80, v81
	v_cvt_pk_f16_f32 v38, v78, v79
	v_mad_u32_u24 v40, v46, s10, v35
	v_lshrrev_b32_e32 v47, 6, v184
	ds_write_b64 v40, v[38:39]
	v_cvt_pk_f16_f32 v39, v76, v77
	v_cvt_pk_f16_f32 v38, v74, v75
	v_mad_u32_u24 v40, v47, s10, v35
	v_lshrrev_b32_e32 v48, 6, v1
	ds_write_b64 v40, v[38:39]
	v_cvt_pk_f16_f32 v39, v72, v73
	v_cvt_pk_f16_f32 v38, v70, v71
	v_mad_u32_u24 v40, v48, s10, v35
	v_lshrrev_b32_e32 v49, 6, v183
	v_lshlrev_b32_e32 v207, 2, v208
	ds_write_b64 v40, v[38:39]
	v_cvt_pk_f16_f32 v39, v68, v69
	v_cvt_pk_f16_f32 v38, v66, v67
	v_mad_u32_u24 v35, v49, s10, v35
	v_lshl_or_b32 v191, v209, 5, v207
	ds_write_b64 v35, v[38:39]
	v_lshl_add_u32 v35, v191, 2, s9
	s_waitcnt lgkmcnt(0)
	s_barrier
	ds_read_b128 v[38:41], v35
	v_or_b32_e32 v194, 8, v191
	s_mov_b32 s15, 0x9000
	v_or_b32_e32 v200, 16, v191
	v_or_b32_e32 v201, 24, v191
	s_waitcnt lgkmcnt(0)
	v_add_f32_e32 v18, v38, v18
	v_cvt_f16_f32_e32 v35, v18
	v_mov_b32_e32 v18, v19
	v_mov_b32_e32 v19, v20
	v_add_f32_e32 v20, v41, v21
	v_cvt_f16_f32_e32 v20, v20
	v_mov_b32_e32 v42, v39
	v_mov_b32_e32 v43, v40
	v_pk_add_f32 v[18:19], v[42:43], v[18:19]
	v_add_f32_e32 v2, v38, v2
	v_cvt_pk_f16_f32 v19, v18, v19
	v_pack_b32_f16 v18, v35, v19
	v_alignbit_b32 v19, v20, v19, 16
	v_lshl_add_u32 v35, v191, 1, v189
	ds_write_b64 v35, v[18:19] offset:512
	v_cvt_f16_f32_e32 v18, v2
	v_mov_b32_e32 v2, v3
	v_mov_b32_e32 v3, v4
	v_add_f32_e32 v4, v41, v5
	v_cvt_f16_f32_e32 v4, v4
	v_pk_add_f32 v[2:3], v[42:43], v[2:3]
	v_mov_b32_e32 v19, v24
	v_cvt_pk_f16_f32 v3, v2, v3
	v_pack_b32_f16 v2, v18, v3
	v_alignbit_b32 v3, v4, v3, 16
	ds_write_b64 v35, v[2:3] offset:33792
	v_lshl_add_u32 v2, v194, 2, s9
	ds_read_b128 v[2:5], v2
	v_add_co_u32_e32 v24, vcc, s15, v180
	v_mul_u32_u24_e32 v199, 0x410, v209
	v_mul_u32_u24_e32 v198, 0x410, v37
	s_waitcnt lgkmcnt(0)
	v_add_f32_e32 v18, v2, v22
	v_cvt_f16_f32_e32 v20, v18
	v_mov_b32_e32 v38, v3
	v_mov_b32_e32 v39, v4
	v_mov_b32_e32 v18, v23
	v_pk_add_f32 v[18:19], v[38:39], v[18:19]
	v_add_f32_e32 v3, v5, v25
	v_cvt_pk_f16_f32 v4, v18, v19
	v_addc_co_u32_e32 v25, vcc, 0, v181, vcc
	v_pack_b32_f16 v22, v20, v4
	global_load_dwordx4 v[18:21], v[180:181], off
	global_load_dwordx4 v[102:105], v[24:25], off offset:-4096
	v_cvt_f16_f32_e32 v3, v3
	v_add_f32_e32 v2, v2, v6
	v_add_f32_e32 v5, v5, v9
	v_cvt_f16_f32_e32 v5, v5
	v_alignbit_b32 v23, v3, v4, 16
	v_cvt_f16_f32_e32 v4, v2
	v_mov_b32_e32 v2, v7
	v_mov_b32_e32 v3, v8
	v_pk_add_f32 v[2:3], v[38:39], v[2:3]
	ds_write_b64 v35, v[22:23] offset:528
	v_cvt_pk_f16_f32 v3, v2, v3
	v_pack_b32_f16 v2, v4, v3
	v_alignbit_b32 v3, v5, v3, 16
	ds_write_b64 v35, v[2:3] offset:33808
	v_lshl_add_u32 v2, v200, 2, s9
	ds_read_b128 v[2:5], v2
	v_mov_b32_e32 v8, v27
	v_mov_b32_e32 v9, v28
	v_mul_u32_u24_e32 v197, 0x410, v44
	v_mul_u32_u24_e32 v195, 0x410, v45
	s_waitcnt lgkmcnt(0)
	v_add_f32_e32 v6, v2, v26
	v_cvt_f16_f32_e32 v22, v6
	v_mov_b32_e32 v6, v3
	v_add_f32_e32 v3, v5, v29
	v_cvt_f16_f32_e32 v3, v3
	v_mov_b32_e32 v7, v4
	v_pk_add_f32 v[8:9], v[6:7], v[8:9]
	v_add_f32_e32 v2, v2, v10
	v_cvt_pk_f16_f32 v4, v8, v9
	v_add_f32_e32 v5, v5, v13
	v_pack_b32_f16 v8, v22, v4
	v_alignbit_b32 v9, v3, v4, 16
	v_cvt_f16_f32_e32 v4, v2
	v_cvt_f16_f32_e32 v5, v5
	v_mov_b32_e32 v2, v11
	v_mov_b32_e32 v3, v12
	v_pk_add_f32 v[2:3], v[6:7], v[2:3]
	ds_write_b64 v35, v[8:9] offset:544
	v_cvt_pk_f16_f32 v3, v2, v3
	v_pack_b32_f16 v2, v4, v3
	v_alignbit_b32 v3, v5, v3, 16
	ds_write_b64 v35, v[2:3] offset:33824
	v_lshl_add_u32 v2, v201, 2, s9
	ds_read_b128 v[2:5], v2
	v_mov_b32_e32 v8, v31
	v_mov_b32_e32 v9, v32
	s_mov_b32 s9, 0x8000
	v_mul_u32_u24_e32 v196, 0x410, v46
	s_waitcnt lgkmcnt(0)
	v_add_f32_e32 v6, v2, v30
	v_cvt_f16_f32_e32 v10, v6
	v_mov_b32_e32 v6, v3
	v_add_f32_e32 v3, v5, v33
	v_cvt_f16_f32_e32 v3, v3
	v_mov_b32_e32 v7, v4
	v_pk_add_f32 v[8:9], v[6:7], v[8:9]
	v_add_f32_e32 v2, v2, v14
	v_cvt_pk_f16_f32 v4, v8, v9
	v_add_f32_e32 v5, v5, v17
	v_pack_b32_f16 v8, v10, v4
	v_alignbit_b32 v9, v3, v4, 16
	v_cvt_f16_f32_e32 v4, v2
	v_cvt_f16_f32_e32 v5, v5
	v_mov_b32_e32 v2, v15
	v_mov_b32_e32 v3, v16
	v_pk_add_f32 v[2:3], v[6:7], v[2:3]
	v_mul_u32_u24_e32 v193, 0x410, v47
	v_cvt_pk_f16_f32 v3, v2, v3
	v_pack_b32_f16 v2, v4, v3
	v_alignbit_b32 v3, v5, v3, 16
	ds_write_b64 v35, v[2:3] offset:33840
	v_add_co_u32_e32 v2, vcc, s9, v180
	v_mul_u32_u24_e32 v192, 0x410, v48
	v_mul_u32_u24_e32 v190, 0x410, v49
	v_addc_co_u32_e32 v3, vcc, 0, v181, vcc
	ds_write_b64 v35, v[8:9] offset:560
	global_load_dwordx4 v[106:109], v[180:181], off offset:1024
	global_load_dwordx4 v[110:113], v[2:3], off offset:1024
	global_load_dwordx4 v[122:125], v[180:181], off offset:2048
	global_load_dwordx4 v[126:129], v[2:3], off offset:2048
	global_load_dwordx4 v[130:133], v[180:181], off offset:3072
	global_load_dwordx4 v[134:137], v[2:3], off offset:3072
	v_add_co_u32_e32 v2, vcc, s3, v180
	s_nop 1
	v_addc_co_u32_e32 v3, vcc, 0, v181, vcc
	global_load_dwordx4 v[138:141], v[2:3], off
	global_load_dwordx4 v[142:145], v[24:25], off
	global_load_dwordx4 v[150:153], v[2:3], off offset:1024
	global_load_dwordx4 v[154:157], v[24:25], off offset:1024
	global_load_dwordx4 v[158:161], v[2:3], off offset:2048
	global_load_dwordx4 v[162:165], v[24:25], off offset:2048
	global_load_dwordx4 v[166:169], v[2:3], off offset:3072
	global_load_dwordx4 v[210:213], v[24:25], off offset:3072
	s_waitcnt lgkmcnt(0)
	s_barrier
	s_cmp_lt_u32 s18, 4
	s_cbranch_scc1 .Lmy_ffn_nostag2
	s_sleep 2
.Lmy_ffn_nostag2:
	ds_read_b128 v[2:5], v202
	ds_read_b128 v[114:117], v202 offset:32
	ds_read_b128 v[6:9], v202 offset:33280
	ds_read_b128 v[146:149], v202 offset:33312
	s_add_i32 s9, 0, 0x13400
	v_add3_u32 v204, s9, v36, v34
	s_waitcnt vmcnt(15) lgkmcnt(3)
	v_mfma_f32_32x32x16_f16 v[50:65], v[18:21], v[2:5], 0
	ds_read_b128 v[170:173], v202 offset:64
	ds_read_b128 v[174:177], v202 offset:33344
	ds_read_b128 v[118:121], v204
	ds_read_b128 v[98:101], v204 offset:1024
	s_waitcnt lgkmcnt(5)
	v_mfma_f32_32x32x16_f16 v[34:49], v[18:21], v[6:9], 0
	s_waitcnt vmcnt(14)
	v_mfma_f32_32x32x16_f16 v[18:33], v[102:105], v[2:5], 0
	v_mfma_f32_32x32x16_f16 v[2:17], v[102:105], v[6:9], 0
	s_waitcnt vmcnt(13)
	v_mfma_f32_32x32x16_f16 v[50:65], v[106:109], v[114:117], v[50:65]
	s_waitcnt lgkmcnt(4)
	v_mfma_f32_32x32x16_f16 v[34:49], v[106:109], v[146:149], v[34:49]
	s_waitcnt vmcnt(12)
	v_mfma_f32_32x32x16_f16 v[18:33], v[110:113], v[114:117], v[18:33]
	ds_read_b128 v[214:217], v202 offset:96
	ds_read_b128 v[218:221], v202 offset:33376
	ds_read_b128 v[114:117], v204 offset:2048
	ds_read_b128 v[102:105], v204 offset:3072
	v_mfma_f32_32x32x16_f16 v[2:17], v[110:113], v[146:149], v[2:17]
	s_waitcnt vmcnt(11) lgkmcnt(7)
	v_mfma_f32_32x32x16_f16 v[50:65], v[122:125], v[170:173], v[50:65]
	s_waitcnt lgkmcnt(6)
	v_mfma_f32_32x32x16_f16 v[34:49], v[122:125], v[174:177], v[34:49]
	s_waitcnt vmcnt(10)
	v_mfma_f32_32x32x16_f16 v[18:33], v[126:129], v[170:173], v[18:33]
	ds_read_b128 v[146:149], v202 offset:128
	ds_read_b128 v[170:173], v202 offset:33408
	ds_read_b128 v[122:125], v204 offset:4096
	ds_read_b128 v[106:109], v204 offset:5120
	v_mfma_f32_32x32x16_f16 v[2:17], v[126:129], v[174:177], v[2:17]
	s_waitcnt vmcnt(9) lgkmcnt(7)
	v_mfma_f32_32x32x16_f16 v[50:65], v[130:133], v[214:217], v[50:65]
	s_waitcnt lgkmcnt(6)
	v_mfma_f32_32x32x16_f16 v[34:49], v[130:133], v[218:221], v[34:49]
	ds_read_b128 v[130:133], v202 offset:160
	ds_read_b128 v[174:177], v202 offset:33440
	ds_read_b128 v[126:129], v204 offset:6144
	ds_read_b128 v[110:113], v204 offset:7168
	s_waitcnt vmcnt(8)
	v_mfma_f32_32x32x16_f16 v[18:33], v[134:137], v[214:217], v[18:33]
	v_mfma_f32_32x32x16_f16 v[2:17], v[134:137], v[218:221], v[2:17]
	v_add_co_u32_e32 v226, vcc, s8, v180
	s_mov_b32 s8, 0xb000
	s_nop 0
	v_addc_co_u32_e32 v227, vcc, 0, v181, vcc
	v_add_co_u32_e32 v228, vcc, s8, v180
	s_waitcnt vmcnt(7) lgkmcnt(7)
	v_mfma_f32_32x32x16_f16 v[50:65], v[138:141], v[146:149], v[50:65]
	v_addc_co_u32_e32 v229, vcc, 0, v181, vcc
	s_waitcnt vmcnt(6)
	v_mfma_f32_32x32x16_f16 v[18:33], v[142:145], v[146:149], v[18:33]
	global_load_dwordx4 v[146:149], v[226:227], off
	global_load_dwordx4 v[134:137], v[228:229], off
	s_waitcnt lgkmcnt(6)
	v_mfma_f32_32x32x16_f16 v[34:49], v[138:141], v[170:173], v[34:49]
	ds_read_b128 v[138:141], v202 offset:192
	ds_read_b128 v[214:217], v202 offset:33472
	v_mfma_f32_32x32x16_f16 v[2:17], v[142:145], v[170:173], v[2:17]
	s_waitcnt vmcnt(7) lgkmcnt(5)
	v_mfma_f32_32x32x16_f16 v[50:65], v[150:153], v[130:133], v[50:65]
	s_waitcnt vmcnt(6)
	v_mfma_f32_32x32x16_f16 v[18:33], v[154:157], v[130:133], v[18:33]
	global_load_dwordx4 v[142:145], v[226:227], off offset:1024
	global_load_dwordx4 v[130:133], v[228:229], off offset:1024
	ds_read_b128 v[218:221], v202 offset:224
	ds_read_b128 v[222:225], v202 offset:33504
	s_waitcnt lgkmcnt(6)
	v_mfma_f32_32x32x16_f16 v[34:49], v[150:153], v[174:177], v[34:49]
	v_mfma_f32_32x32x16_f16 v[2:17], v[154:157], v[174:177], v[2:17]
	s_waitcnt vmcnt(7) lgkmcnt(3)
	v_mfma_f32_32x32x16_f16 v[50:65], v[158:161], v[138:141], v[50:65]
	s_waitcnt vmcnt(6)
	v_mfma_f32_32x32x16_f16 v[18:33], v[162:165], v[138:141], v[18:33]
	global_load_dwordx4 v[150:153], v[226:227], off offset:2048
	global_load_dwordx4 v[138:141], v[228:229], off offset:2048
	ds_read_b128 v[174:177], v202 offset:256
	ds_read_b128 v[170:173], v202 offset:33536
	s_waitcnt lgkmcnt(4)
	v_mfma_f32_32x32x16_f16 v[34:49], v[158:161], v[214:217], v[34:49]
	v_mfma_f32_32x32x16_f16 v[2:17], v[162:165], v[214:217], v[2:17]
	global_load_dwordx4 v[158:161], v[226:227], off offset:3072
	global_load_dwordx4 v[154:157], v[228:229], off offset:3072
	s_waitcnt vmcnt(9) lgkmcnt(3)
	v_mfma_f32_32x32x16_f16 v[50:65], v[166:169], v[218:221], v[50:65]
	s_waitcnt lgkmcnt(2)
	v_mfma_f32_32x32x16_f16 v[34:49], v[166:169], v[222:225], v[34:49]
	ds_read_b128 v[166:169], v202 offset:288
	ds_read_b128 v[162:165], v202 offset:33568
	s_waitcnt vmcnt(8)
	v_mfma_f32_32x32x16_f16 v[18:33], v[210:213], v[218:221], v[18:33]
	v_mfma_f32_32x32x16_f16 v[2:17], v[210:213], v[222:225], v[2:17]
	s_mov_b64 s[8:9], 0x4000
	v_add_u32_e32 v203, 0x140, v202
	v_lshl_add_u64 v[180:181], v[180:181], 0, s[8:9]
	s_mov_b64 s[8:9], 0x8000
	s_mov_b64 s[10:11], 0x1000
	s_mov_b64 s[12:13], 0x9000
	v_mov_b32_e32 v210, v203

.LBB3_24:
	s_or_b64 exec, exec, s[6:7]
	v_lshl_add_u32 v10, v205, 3, 0
	s_waitcnt lgkmcnt(3)
	v_add_u32_e32 v14, 0x10400, v10
	s_waitcnt lgkmcnt(0)
	s_barrier
	ds_read2_b64 v[10:13], v14 offset1:32
	ds_read2_b64 v[28:31], v14 offset0:64 offset1:96
	ds_read2_b64 v[62:65], v14 offset0:128 offset1:160
	ds_read2_b64 v[152:155], v14 offset0:192 offset1:224
	v_add_u32_e32 v14, 0x800, v14
	s_waitcnt lgkmcnt(3)
	v_pk_add_f32 v[10:11], v[10:11], 0 op_sel_hi:[1,0]
	ds_read2_b64 v[156:159], v14 offset1:32
	ds_read2_b64 v[160:163], v14 offset0:64 offset1:96
	ds_read2_b64 v[164:167], v14 offset0:128 offset1:160
	ds_read2_b64 v[168:171], v14 offset0:192 offset1:224
	s_waitcnt lgkmcnt(6)
	v_pk_add_f32 v[10:11], v[10:11], v[28:29]
	s_mov_b32 s6, 0x3b000000
	s_waitcnt lgkmcnt(5)
	v_pk_add_f32 v[10:11], v[10:11], v[62:63]
	s_add_i32 s11, 0, 0x12800
	s_waitcnt lgkmcnt(4)
	v_pk_add_f32 v[10:11], v[10:11], v[152:153]
	s_mov_b32 s10, 0x3e6d3388
	s_waitcnt lgkmcnt(3)
	v_pk_add_f32 v[10:11], v[10:11], v[156:157]
	s_mov_b32 s8, 0xbf3a00e3
	s_waitcnt lgkmcnt(2)
	v_pk_add_f32 v[10:11], v[10:11], v[160:161]
	s_mov_b32 s14, 0xbf38aa3b
	s_waitcnt lgkmcnt(1)
	v_pk_add_f32 v[10:11], v[10:11], v[164:165]
	s_mov_b32 s12, 0x3f35f0e3
	s_waitcnt lgkmcnt(0)
	v_pk_add_f32 v[10:11], v[10:11], v[168:169]
	s_mov_b32 s16, 0x3e027906
	v_pk_mul_f32 v[16:17], v[10:11], s[6:7] op_sel_hi:[1,0]
	s_nop 0
	v_fma_f32 v10, -v16, v16, v17
	v_add_f32_e32 v10, 0x3727c5ac, v10
	v_rsq_f32_e32 v22, v10
	v_pk_add_f32 v[10:11], v[12:13], 0 op_sel_hi:[1,0]
	v_or_b32_e32 v13, v151, v207
	v_pk_add_f32 v[10:11], v[10:11], v[30:31]
	v_lshlrev_b32_e32 v23, 2, v13
	v_pk_add_f32 v[10:11], v[10:11], v[64:65]
	v_add_u32_e32 v15, s11, v23
	v_pk_add_f32 v[10:11], v[10:11], v[154:155]
	v_pk_add_f32 v[146:147], v[146:147], v[16:17] op_sel_hi:[1,0] neg_lo:[0,1] neg_hi:[0,1]
	v_pk_add_f32 v[10:11], v[10:11], v[158:159]
	v_pk_mul_f32 v[146:147], v[146:147], v[22:23] op_sel_hi:[1,0]
	v_pk_add_f32 v[10:11], v[10:11], v[162:163]
	v_lshlrev_b32_e32 v13, 1, v13
	v_pk_add_f32 v[10:11], v[10:11], v[166:167]
	v_pk_add_f32 v[138:139], v[138:139], v[16:17] op_sel_hi:[1,0] neg_lo:[0,1] neg_hi:[0,1]
	v_pk_add_f32 v[10:11], v[10:11], v[170:171]
	v_pk_mul_f32 v[138:139], v[138:139], v[22:23] op_sel_hi:[1,0]
	v_pk_mul_f32 v[10:11], v[10:11], s[6:7] op_sel_hi:[1,0]
	s_add_i32 s7, 0, 0x12000
	v_add_u32_e32 v14, s7, v23
	ds_read_b128 v[28:31], v14
	ds_read_b128 v[62:65], v15
	v_pk_add_f32 v[14:15], v[148:149], v[16:17] op_sel_hi:[1,0] neg_lo:[0,1] neg_hi:[0,1]
	s_mov_b32 s6, 0x3f07dc22
	v_pk_mul_f32 v[14:15], v[14:15], v[22:23] op_sel_hi:[1,0]
	v_fma_f32 v12, -v10, v10, v11
	s_waitcnt lgkmcnt(0)
	v_pk_fma_f32 v[32:33], v[28:29], v[14:15], v[62:63]
	v_pk_fma_f32 v[146:147], v[30:31], v[146:147], v[64:65]
	v_and_b32_e32 v15, 0x7fffffff, v33
	v_and_b32_e32 v14, 0x7fffffff, v32
	v_pk_fma_f32 v[14:15], v[14:15], s[10:11], 1.0 op_sel_hi:[1,0,0]
	v_pk_mul_f32 v[154:155], v[32:33], v[32:33]
	v_rcp_f32_e32 v148, v14
	v_rcp_f32_e32 v149, v15
	v_mov_b64_e32 v[14:15], s[8:9]
	v_pk_mul_f32 v[154:155], v[154:155], s[14:15] op_sel_hi:[1,0]
	s_mov_b32 s8, 0xbe11a98e
	v_pk_fma_f32 v[152:153], v[148:149], s[6:7], v[14:15] op_sel_hi:[1,0,0]
	v_exp_f32_e32 v154, v154
	v_pk_fma_f32 v[152:153], v[148:149], v[152:153], s[12:13] op_sel_hi:[1,1,0]
	v_exp_f32_e32 v155, v155
	v_pk_fma_f32 v[152:153], v[148:149], v[152:153], s[8:9] op_sel_hi:[1,1,0]
	v_add_f32_e32 v12, 0x3727c5ac, v12
	v_pk_fma_f32 v[152:153], v[148:149], v[152:153], s[16:17] op_sel_hi:[1,1,0]
	v_cmp_gt_f32_e32 vcc, 0, v33
	v_pk_mul_f32 v[148:149], v[148:149], v[152:153]
	v_rsq_f32_e32 v12, v12
	v_pk_mul_f32 v[148:149], v[154:155], v[148:149]
	v_and_b32_e32 v155, 0x7fffffff, v147
	v_and_b32_e32 v154, 0x7fffffff, v146
	v_pk_fma_f32 v[154:155], v[154:155], s[10:11], 1.0 op_sel_hi:[1,0,0]
	v_pk_mul_f32 v[152:153], v[32:33], v[148:149]
	v_rcp_f32_e32 v154, v154
	v_rcp_f32_e32 v155, v155
	v_pk_fma_f32 v[148:149], v[32:33], v[148:149], v[32:33] neg_lo:[1,0,0] neg_hi:[1,0,0]
	v_pk_add_f32 v[144:145], v[144:145], v[10:11] op_sel_hi:[1,0] neg_lo:[0,1] neg_hi:[0,1]
	v_cndmask_b32_e32 v33, v149, v153, vcc
	v_cmp_gt_f32_e32 vcc, 0, v32
	v_pk_mul_f32 v[144:145], v[144:145], v[12:13] op_sel_hi:[1,0]
	v_add3_u32 v13, 0, v13, v187
	v_cndmask_b32_e32 v32, v148, v152, vcc
	v_pk_mul_f32 v[152:153], v[146:147], v[146:147]
	v_pk_fma_f32 v[148:149], v[154:155], s[6:7], v[14:15] op_sel_hi:[1,0,0]
	v_pk_mul_f32 v[152:153], v[152:153], s[14:15] op_sel_hi:[1,0]
	v_pk_fma_f32 v[148:149], v[154:155], v[148:149], s[12:13] op_sel_hi:[1,1,0]
	v_exp_f32_e32 v152, v152
	v_exp_f32_e32 v153, v153
	v_pk_fma_f32 v[148:149], v[154:155], v[148:149], s[8:9] op_sel_hi:[1,1,0]
	v_pk_fma_f32 v[28:29], v[28:29], v[144:145], v[62:63]
	v_pk_fma_f32 v[148:149], v[154:155], v[148:149], s[16:17] op_sel_hi:[1,1,0]
	v_and_b32_e32 v63, 0x7fffffff, v29
	v_pk_mul_f32 v[148:149], v[154:155], v[148:149]
	v_and_b32_e32 v62, 0x7fffffff, v28
	v_pk_mul_f32 v[148:149], v[152:153], v[148:149]
	v_pk_fma_f32 v[62:63], v[62:63], s[10:11], 1.0 op_sel_hi:[1,0,0]
	v_pk_mul_f32 v[152:153], v[146:147], v[148:149]
	v_pk_fma_f32 v[148:149], v[146:147], v[148:149], v[146:147] neg_lo:[1,0,0] neg_hi:[1,0,0]
	v_cmp_gt_f32_e32 vcc, 0, v147
	v_rcp_f32_e32 v62, v62
	v_rcp_f32_e32 v63, v63
	v_cvt_pk_f16_f32 v32, v32, v33
	v_cndmask_b32_e32 v33, v149, v153, vcc
	v_cmp_gt_f32_e32 vcc, 0, v146
	v_pk_mul_f32 v[144:145], v[28:29], v[28:29]
	v_pk_add_f32 v[142:143], v[142:143], v[10:11] op_sel_hi:[1,0] neg_lo:[0,1] neg_hi:[0,1]
	v_cndmask_b32_e32 v146, v148, v152, vcc
	v_cvt_pk_f16_f32 v33, v146, v33
	ds_write_b64 v13, v[32:33]
	v_pk_fma_f32 v[32:33], v[62:63], s[6:7], v[14:15] op_sel_hi:[1,0,0]
	v_pk_mul_f32 v[144:145], v[144:145], s[14:15] op_sel_hi:[1,0]
	v_pk_fma_f32 v[32:33], v[62:63], v[32:33], s[12:13] op_sel_hi:[1,1,0]
	v_exp_f32_e32 v144, v144
	v_exp_f32_e32 v145, v145
	v_pk_mul_f32 v[142:143], v[142:143], v[12:13] op_sel_hi:[1,0]
	v_pk_fma_f32 v[32:33], v[62:63], v[32:33], s[8:9] op_sel_hi:[1,1,0]
	v_pk_fma_f32 v[30:31], v[30:31], v[142:143], v[64:65]
	v_pk_fma_f32 v[32:33], v[62:63], v[32:33], s[16:17] op_sel_hi:[1,1,0]
	v_and_b32_e32 v65, 0x7fffffff, v31
	v_and_b32_e32 v64, 0x7fffffff, v30
	v_pk_mul_f32 v[32:33], v[62:63], v[32:33]
	v_pk_fma_f32 v[64:65], v[64:65], s[10:11], 1.0 op_sel_hi:[1,0,0]
	v_pk_mul_f32 v[32:33], v[144:145], v[32:33]
	v_rcp_f32_e32 v64, v64
	v_rcp_f32_e32 v65, v65
	v_pk_mul_f32 v[62:63], v[28:29], v[32:33]
	v_pk_fma_f32 v[32:33], v[28:29], v[32:33], v[28:29] neg_lo:[1,0,0] neg_hi:[1,0,0]
	v_cmp_gt_f32_e32 vcc, 0, v29
	v_pk_add_f32 v[136:137], v[136:137], v[10:11] op_sel_hi:[1,0] neg_lo:[0,1] neg_hi:[0,1]
	v_pk_add_f32 v[132:133], v[132:133], v[10:11] op_sel_hi:[1,0] neg_lo:[0,1] neg_hi:[0,1]
	v_cndmask_b32_e32 v29, v33, v63, vcc
	v_cmp_gt_f32_e32 vcc, 0, v28
	v_pk_mul_f32 v[136:137], v[136:137], v[12:13] op_sel_hi:[1,0]
	v_pk_mul_f32 v[132:133], v[132:133], v[12:13] op_sel_hi:[1,0]
	v_cndmask_b32_e32 v28, v32, v62, vcc
	v_pk_mul_f32 v[62:63], v[30:31], v[30:31]
	v_pk_fma_f32 v[32:33], v[64:65], s[6:7], v[14:15] op_sel_hi:[1,0,0]
	v_pk_mul_f32 v[62:63], v[62:63], s[14:15] op_sel_hi:[1,0]
	v_pk_fma_f32 v[32:33], v[64:65], v[32:33], s[12:13] op_sel_hi:[1,1,0]
	v_exp_f32_e32 v62, v62
	v_exp_f32_e32 v63, v63
	v_pk_fma_f32 v[32:33], v[64:65], v[32:33], s[8:9] op_sel_hi:[1,1,0]
	v_cmp_gt_f32_e32 vcc, 0, v31
	v_pk_fma_f32 v[32:33], v[64:65], v[32:33], s[16:17] op_sel_hi:[1,1,0]
	v_cvt_pk_f16_f32 v28, v28, v29
	v_pk_mul_f32 v[32:33], v[64:65], v[32:33]
	v_pk_add_f32 v[130:131], v[130:131], v[16:17] op_sel_hi:[1,0] neg_lo:[0,1] neg_hi:[0,1]
	v_pk_mul_f32 v[32:33], v[62:63], v[32:33]
	v_pk_mul_f32 v[130:131], v[130:131], v[22:23] op_sel_hi:[1,0]
	v_pk_mul_f32 v[62:63], v[30:31], v[32:33]
	v_pk_fma_f32 v[32:33], v[30:31], v[32:33], v[30:31] neg_lo:[1,0,0] neg_hi:[1,0,0]
	v_pk_add_f32 v[60:61], v[60:61], v[10:11] op_sel_hi:[1,0] neg_lo:[0,1] neg_hi:[0,1]
	v_cndmask_b32_e32 v29, v33, v63, vcc
	v_cmp_gt_f32_e32 vcc, 0, v30
	v_pk_mul_f32 v[60:61], v[60:61], v[12:13] op_sel_hi:[1,0]
	v_pk_add_f32 v[58:59], v[58:59], v[10:11] op_sel_hi:[1,0] neg_lo:[0,1] neg_hi:[0,1]
	v_cndmask_b32_e32 v30, v32, v62, vcc
	v_cvt_pk_f16_f32 v29, v30, v29
	ds_write_b64 v13, v[28:29] offset:33280
	v_or_b32_e32 v28, 32, v23
	v_add_u32_e32 v29, s7, v28
	v_add_u32_e32 v32, s11, v28
	ds_read_b128 v[28:31], v29
	ds_read_b128 v[62:65], v32
	v_pk_add_f32 v[32:33], v[140:141], v[16:17] op_sel_hi:[1,0] neg_lo:[0,1] neg_hi:[0,1]
	v_pk_mul_f32 v[58:59], v[58:59], v[12:13] op_sel_hi:[1,0]
	v_pk_mul_f32 v[32:33], v[32:33], v[22:23] op_sel_hi:[1,0]
	v_pk_add_f32 v[54:55], v[54:55], v[16:17] op_sel_hi:[1,0] neg_lo:[0,1] neg_hi:[0,1]
	s_waitcnt lgkmcnt(0)
	v_pk_fma_f32 v[32:33], v[28:29], v[32:33], v[62:63]
	v_pk_fma_f32 v[138:139], v[30:31], v[138:139], v[64:65]
	v_and_b32_e32 v141, 0x7fffffff, v33
	v_and_b32_e32 v140, 0x7fffffff, v32
	v_pk_fma_f32 v[140:141], v[140:141], s[10:11], 1.0 op_sel_hi:[1,0,0]
	v_pk_mul_f32 v[144:145], v[32:33], v[32:33]
	v_rcp_f32_e32 v140, v140
	v_rcp_f32_e32 v141, v141
	v_pk_mul_f32 v[144:145], v[144:145], s[14:15] op_sel_hi:[1,0]
	v_cmp_gt_f32_e32 vcc, 0, v33
	v_exp_f32_e32 v144, v144
	v_pk_fma_f32 v[142:143], v[140:141], s[6:7], v[14:15] op_sel_hi:[1,0,0]
	v_exp_f32_e32 v145, v145
	v_pk_fma_f32 v[142:143], v[140:141], v[142:143], s[12:13] op_sel_hi:[1,1,0]
	v_pk_fma_f32 v[28:29], v[28:29], v[136:137], v[62:63]
	v_pk_fma_f32 v[142:143], v[140:141], v[142:143], s[8:9] op_sel_hi:[1,1,0]
	v_and_b32_e32 v63, 0x7fffffff, v29
	v_pk_fma_f32 v[142:143], v[140:141], v[142:143], s[16:17] op_sel_hi:[1,1,0]
	v_and_b32_e32 v62, 0x7fffffff, v28
	v_pk_mul_f32 v[140:141], v[140:141], v[142:143]
	v_pk_fma_f32 v[62:63], v[62:63], s[10:11], 1.0 op_sel_hi:[1,0,0]
	v_pk_mul_f32 v[140:141], v[144:145], v[140:141]
	v_and_b32_e32 v145, 0x7fffffff, v139
	v_and_b32_e32 v144, 0x7fffffff, v138
	v_pk_fma_f32 v[144:145], v[144:145], s[10:11], 1.0 op_sel_hi:[1,0,0]
	v_pk_mul_f32 v[142:143], v[32:33], v[140:141]
	v_rcp_f32_e32 v144, v144
	v_rcp_f32_e32 v145, v145
	v_pk_fma_f32 v[140:141], v[32:33], v[140:141], v[32:33] neg_lo:[1,0,0] neg_hi:[1,0,0]
	v_rcp_f32_e32 v62, v62
	v_cndmask_b32_e32 v33, v141, v143, vcc
	v_cmp_gt_f32_e32 vcc, 0, v32
	v_rcp_f32_e32 v63, v63
	v_pk_fma_f32 v[30:31], v[30:31], v[132:133], v[64:65]
	v_cndmask_b32_e32 v32, v140, v142, vcc
	v_pk_mul_f32 v[142:143], v[138:139], v[138:139]
	v_pk_fma_f32 v[140:141], v[144:145], s[6:7], v[14:15] op_sel_hi:[1,0,0]
	v_pk_mul_f32 v[142:143], v[142:143], s[14:15] op_sel_hi:[1,0]
	v_pk_fma_f32 v[140:141], v[144:145], v[140:141], s[12:13] op_sel_hi:[1,1,0]
	v_exp_f32_e32 v142, v142
	v_exp_f32_e32 v143, v143
	v_pk_fma_f32 v[140:141], v[144:145], v[140:141], s[8:9] op_sel_hi:[1,1,0]
	v_cmp_gt_f32_e32 vcc, 0, v139
	v_pk_fma_f32 v[140:141], v[144:145], v[140:141], s[16:17] op_sel_hi:[1,1,0]
	v_cvt_pk_f16_f32 v32, v32, v33
	v_pk_mul_f32 v[140:141], v[144:145], v[140:141]
	v_and_b32_e32 v65, 0x7fffffff, v31
	v_pk_mul_f32 v[140:141], v[142:143], v[140:141]
	v_and_b32_e32 v64, 0x7fffffff, v30
	v_pk_mul_f32 v[142:143], v[138:139], v[140:141]
	v_pk_fma_f32 v[140:141], v[138:139], v[140:141], v[138:139] neg_lo:[1,0,0] neg_hi:[1,0,0]
	v_pk_fma_f32 v[64:65], v[64:65], s[10:11], 1.0 op_sel_hi:[1,0,0]
	v_cndmask_b32_e32 v33, v141, v143, vcc
	v_cmp_gt_f32_e32 vcc, 0, v138
	v_rcp_f32_e32 v64, v64
	v_rcp_f32_e32 v65, v65
	v_cndmask_b32_e32 v136, v140, v142, vcc
	v_cvt_pk_f16_f32 v33, v136, v33
	v_pk_mul_f32 v[136:137], v[28:29], v[28:29]
	ds_write_b64 v13, v[32:33] offset:16
	v_pk_fma_f32 v[32:33], v[62:63], s[6:7], v[14:15] op_sel_hi:[1,0,0]
	v_pk_mul_f32 v[136:137], v[136:137], s[14:15] op_sel_hi:[1,0]
	v_pk_fma_f32 v[32:33], v[62:63], v[32:33], s[12:13] op_sel_hi:[1,1,0]
	v_exp_f32_e32 v136, v136
	v_exp_f32_e32 v137, v137
	v_pk_fma_f32 v[32:33], v[62:63], v[32:33], s[8:9] op_sel_hi:[1,1,0]
	v_cmp_gt_f32_e32 vcc, 0, v29
	v_pk_fma_f32 v[32:33], v[62:63], v[32:33], s[16:17] op_sel_hi:[1,1,0]
	v_pk_mul_f32 v[54:55], v[54:55], v[22:23] op_sel_hi:[1,0]
	v_pk_mul_f32 v[32:33], v[62:63], v[32:33]
	v_pk_add_f32 v[52:53], v[52:53], v[10:11] op_sel_hi:[1,0] neg_lo:[0,1] neg_hi:[0,1]
	v_pk_mul_f32 v[32:33], v[136:137], v[32:33]
	v_pk_mul_f32 v[52:53], v[52:53], v[12:13] op_sel_hi:[1,0]
	v_pk_mul_f32 v[62:63], v[28:29], v[32:33]
	v_pk_fma_f32 v[32:33], v[28:29], v[32:33], v[28:29] neg_lo:[1,0,0] neg_hi:[1,0,0]
	v_pk_add_f32 v[50:51], v[50:51], v[10:11] op_sel_hi:[1,0] neg_lo:[0,1] neg_hi:[0,1]
	v_cndmask_b32_e32 v29, v33, v63, vcc
	v_cmp_gt_f32_e32 vcc, 0, v28
	v_pk_mul_f32 v[50:51], v[50:51], v[12:13] op_sel_hi:[1,0]
	v_pk_add_f32 v[46:47], v[46:47], v[16:17] op_sel_hi:[1,0] neg_lo:[0,1] neg_hi:[0,1]
	v_cndmask_b32_e32 v28, v32, v62, vcc
	v_pk_mul_f32 v[62:63], v[30:31], v[30:31]
	v_pk_fma_f32 v[32:33], v[64:65], s[6:7], v[14:15] op_sel_hi:[1,0,0]
	v_pk_mul_f32 v[62:63], v[62:63], s[14:15] op_sel_hi:[1,0]
	v_pk_fma_f32 v[32:33], v[64:65], v[32:33], s[12:13] op_sel_hi:[1,1,0]
	v_exp_f32_e32 v62, v62
	v_exp_f32_e32 v63, v63
	v_pk_fma_f32 v[32:33], v[64:65], v[32:33], s[8:9] op_sel_hi:[1,1,0]
	v_cmp_gt_f32_e32 vcc, 0, v31
	v_pk_fma_f32 v[32:33], v[64:65], v[32:33], s[16:17] op_sel_hi:[1,1,0]
	v_cvt_pk_f16_f32 v28, v28, v29
	v_pk_mul_f32 v[32:33], v[64:65], v[32:33]
	v_pk_mul_f32 v[46:47], v[46:47], v[22:23] op_sel_hi:[1,0]
	v_pk_mul_f32 v[32:33], v[62:63], v[32:33]
	v_pk_add_f32 v[44:45], v[44:45], v[10:11] op_sel_hi:[1,0] neg_lo:[0,1] neg_hi:[0,1]
	v_pk_mul_f32 v[62:63], v[30:31], v[32:33]
	v_pk_fma_f32 v[32:33], v[30:31], v[32:33], v[30:31] neg_lo:[1,0,0] neg_hi:[1,0,0]
	v_pk_mul_f32 v[44:45], v[44:45], v[12:13] op_sel_hi:[1,0]
	v_cndmask_b32_e32 v29, v33, v63, vcc
	v_cmp_gt_f32_e32 vcc, 0, v30
	v_pk_add_f32 v[42:43], v[42:43], v[10:11] op_sel_hi:[1,0] neg_lo:[0,1] neg_hi:[0,1]
	v_pk_add_f32 v[38:39], v[38:39], v[16:17] op_sel_hi:[1,0] neg_lo:[0,1] neg_hi:[0,1]
	v_cndmask_b32_e32 v30, v32, v62, vcc
	v_cvt_pk_f16_f32 v29, v30, v29
	ds_write_b64 v13, v[28:29] offset:33296
	v_or_b32_e32 v28, 64, v23
	v_add_u32_e32 v29, s7, v28
	v_add_u32_e32 v32, s11, v28
	ds_read_b128 v[28:31], v29
	ds_read_b128 v[62:65], v32
	v_pk_add_f32 v[32:33], v[134:135], v[16:17] op_sel_hi:[1,0] neg_lo:[0,1] neg_hi:[0,1]
	v_pk_mul_f32 v[42:43], v[42:43], v[12:13] op_sel_hi:[1,0]
	v_pk_mul_f32 v[32:33], v[32:33], v[22:23] op_sel_hi:[1,0]
	v_pk_mul_f32 v[38:39], v[38:39], v[22:23] op_sel_hi:[1,0]
	s_waitcnt lgkmcnt(0)
	v_pk_fma_f32 v[32:33], v[28:29], v[32:33], v[62:63]
	v_pk_fma_f32 v[130:131], v[30:31], v[130:131], v[64:65]
	v_and_b32_e32 v133, 0x7fffffff, v33
	v_and_b32_e32 v132, 0x7fffffff, v32
	v_pk_fma_f32 v[132:133], v[132:133], s[10:11], 1.0 op_sel_hi:[1,0,0]
	v_pk_mul_f32 v[136:137], v[32:33], v[32:33]
	v_rcp_f32_e32 v132, v132
	v_rcp_f32_e32 v133, v133
	v_pk_mul_f32 v[136:137], v[136:137], s[14:15] op_sel_hi:[1,0]
	v_cmp_gt_f32_e32 vcc, 0, v33
	v_exp_f32_e32 v136, v136
	v_pk_fma_f32 v[134:135], v[132:133], s[6:7], v[14:15] op_sel_hi:[1,0,0]
	v_exp_f32_e32 v137, v137
	v_pk_fma_f32 v[134:135], v[132:133], v[134:135], s[12:13] op_sel_hi:[1,1,0]
	v_pk_fma_f32 v[28:29], v[28:29], v[60:61], v[62:63]
	v_pk_fma_f32 v[134:135], v[132:133], v[134:135], s[8:9] op_sel_hi:[1,1,0]
	v_and_b32_e32 v61, 0x7fffffff, v29
	v_pk_fma_f32 v[134:135], v[132:133], v[134:135], s[16:17] op_sel_hi:[1,1,0]
	v_and_b32_e32 v60, 0x7fffffff, v28
	v_pk_mul_f32 v[132:133], v[132:133], v[134:135]
	v_pk_fma_f32 v[60:61], v[60:61], s[10:11], 1.0 op_sel_hi:[1,0,0]
	v_pk_mul_f32 v[132:133], v[136:137], v[132:133]
	v_and_b32_e32 v137, 0x7fffffff, v131
	v_and_b32_e32 v136, 0x7fffffff, v130
	v_pk_fma_f32 v[136:137], v[136:137], s[10:11], 1.0 op_sel_hi:[1,0,0]
	v_pk_mul_f32 v[134:135], v[32:33], v[132:133]
	v_rcp_f32_e32 v136, v136
	v_rcp_f32_e32 v137, v137
	v_pk_fma_f32 v[132:133], v[32:33], v[132:133], v[32:33] neg_lo:[1,0,0] neg_hi:[1,0,0]
	v_rcp_f32_e32 v60, v60
	v_cndmask_b32_e32 v33, v133, v135, vcc
	v_cmp_gt_f32_e32 vcc, 0, v32
	v_rcp_f32_e32 v61, v61
	v_pk_fma_f32 v[30:31], v[30:31], v[58:59], v[64:65]
	v_cndmask_b32_e32 v32, v132, v134, vcc
	v_pk_mul_f32 v[134:135], v[130:131], v[130:131]
	v_pk_fma_f32 v[132:133], v[136:137], s[6:7], v[14:15] op_sel_hi:[1,0,0]
	v_pk_mul_f32 v[134:135], v[134:135], s[14:15] op_sel_hi:[1,0]
	v_pk_fma_f32 v[132:133], v[136:137], v[132:133], s[12:13] op_sel_hi:[1,1,0]
	v_exp_f32_e32 v134, v134
	v_exp_f32_e32 v135, v135
	v_pk_fma_f32 v[132:133], v[136:137], v[132:133], s[8:9] op_sel_hi:[1,1,0]
	v_cmp_gt_f32_e32 vcc, 0, v131
	v_pk_fma_f32 v[132:133], v[136:137], v[132:133], s[16:17] op_sel_hi:[1,1,0]
	v_cvt_pk_f16_f32 v32, v32, v33
	v_pk_mul_f32 v[132:133], v[136:137], v[132:133]
	v_and_b32_e32 v59, 0x7fffffff, v31
	v_pk_mul_f32 v[132:133], v[134:135], v[132:133]
	v_and_b32_e32 v58, 0x7fffffff, v30
	v_pk_mul_f32 v[134:135], v[130:131], v[132:133]
	v_pk_fma_f32 v[132:133], v[130:131], v[132:133], v[130:131] neg_lo:[1,0,0] neg_hi:[1,0,0]
	v_pk_fma_f32 v[58:59], v[58:59], s[10:11], 1.0 op_sel_hi:[1,0,0]
	v_cndmask_b32_e32 v33, v133, v135, vcc
	v_cmp_gt_f32_e32 vcc, 0, v130
	v_rcp_f32_e32 v58, v58
	v_rcp_f32_e32 v59, v59
	v_cndmask_b32_e32 v62, v132, v134, vcc
	v_cvt_pk_f16_f32 v33, v62, v33
	v_pk_mul_f32 v[62:63], v[28:29], v[28:29]
	ds_write_b64 v13, v[32:33] offset:32
	v_pk_fma_f32 v[32:33], v[60:61], s[6:7], v[14:15] op_sel_hi:[1,0,0]
	v_pk_mul_f32 v[62:63], v[62:63], s[14:15] op_sel_hi:[1,0]
	v_pk_fma_f32 v[32:33], v[60:61], v[32:33], s[12:13] op_sel_hi:[1,1,0]
	v_exp_f32_e32 v62, v62
	v_exp_f32_e32 v63, v63
	v_pk_fma_f32 v[32:33], v[60:61], v[32:33], s[8:9] op_sel_hi:[1,1,0]
	v_cmp_gt_f32_e32 vcc, 0, v29
	v_pk_fma_f32 v[32:33], v[60:61], v[32:33], s[16:17] op_sel_hi:[1,1,0]
	v_pk_add_f32 v[36:37], v[36:37], v[10:11] op_sel_hi:[1,0] neg_lo:[0,1] neg_hi:[0,1]
	v_pk_mul_f32 v[32:33], v[60:61], v[32:33]
	v_pk_mul_f32 v[36:37], v[36:37], v[12:13] op_sel_hi:[1,0]
	v_pk_mul_f32 v[32:33], v[62:63], v[32:33]
	v_pk_add_f32 v[34:35], v[34:35], v[10:11] op_sel_hi:[1,0] neg_lo:[0,1] neg_hi:[0,1]
	v_pk_mul_f32 v[60:61], v[28:29], v[32:33]
	v_pk_fma_f32 v[32:33], v[28:29], v[32:33], v[28:29] neg_lo:[1,0,0] neg_hi:[1,0,0]
	v_pk_mul_f32 v[34:35], v[34:35], v[12:13] op_sel_hi:[1,0]
	v_cndmask_b32_e32 v29, v33, v61, vcc
	v_cmp_gt_f32_e32 vcc, 0, v28
	v_pk_add_f32 v[26:27], v[26:27], v[16:17] op_sel_hi:[1,0] neg_lo:[0,1] neg_hi:[0,1]
	v_pk_add_f32 v[24:25], v[24:25], v[16:17] op_sel_hi:[1,0] neg_lo:[0,1] neg_hi:[0,1]
	v_cndmask_b32_e32 v28, v32, v60, vcc
	v_pk_mul_f32 v[60:61], v[30:31], v[30:31]
	v_pk_fma_f32 v[32:33], v[58:59], s[6:7], v[14:15] op_sel_hi:[1,0,0]
	v_pk_mul_f32 v[60:61], v[60:61], s[14:15] op_sel_hi:[1,0]
	v_pk_fma_f32 v[32:33], v[58:59], v[32:33], s[12:13] op_sel_hi:[1,1,0]
	v_exp_f32_e32 v60, v60
	v_exp_f32_e32 v61, v61
	v_pk_fma_f32 v[32:33], v[58:59], v[32:33], s[8:9] op_sel_hi:[1,1,0]
	v_cmp_gt_f32_e32 vcc, 0, v31
	v_pk_fma_f32 v[32:33], v[58:59], v[32:33], s[16:17] op_sel_hi:[1,1,0]
	v_cvt_pk_f16_f32 v28, v28, v29
	v_pk_mul_f32 v[32:33], v[58:59], v[32:33]
	v_pk_mul_f32 v[26:27], v[26:27], v[22:23] op_sel_hi:[1,0]
	v_pk_mul_f32 v[32:33], v[60:61], v[32:33]
	v_pk_mul_f32 v[24:25], v[24:25], v[22:23] op_sel_hi:[1,0]
	v_pk_mul_f32 v[58:59], v[30:31], v[32:33]
	v_pk_fma_f32 v[32:33], v[30:31], v[32:33], v[30:31] neg_lo:[1,0,0] neg_hi:[1,0,0]
	v_pk_add_f32 v[20:21], v[20:21], v[10:11] op_sel_hi:[1,0] neg_lo:[0,1] neg_hi:[0,1]
	v_cndmask_b32_e32 v29, v33, v59, vcc
	v_cmp_gt_f32_e32 vcc, 0, v30
	v_pk_mul_f32 v[20:21], v[20:21], v[12:13] op_sel_hi:[1,0]
	v_pk_add_f32 v[18:19], v[18:19], v[10:11] op_sel_hi:[1,0] neg_lo:[0,1] neg_hi:[0,1]
	v_cndmask_b32_e32 v30, v32, v58, vcc
	v_cvt_pk_f16_f32 v29, v30, v29
	ds_write_b64 v13, v[28:29] offset:33312
	v_or_b32_e32 v28, 0x60, v23
	v_add_u32_e32 v29, s7, v28
	v_add_u32_e32 v32, s11, v28
	ds_read_b128 v[28:31], v29
	ds_read_b128 v[58:61], v32
	v_pk_add_f32 v[32:33], v[56:57], v[16:17] op_sel_hi:[1,0] neg_lo:[0,1] neg_hi:[0,1]
	v_pk_mul_f32 v[18:19], v[18:19], v[12:13] op_sel_hi:[1,0]
	v_pk_mul_f32 v[32:33], v[32:33], v[22:23] op_sel_hi:[1,0]
	v_pk_add_f32 v[8:9], v[8:9], v[16:17] op_sel_hi:[1,0] neg_lo:[0,1] neg_hi:[0,1]
	s_waitcnt lgkmcnt(0)
	v_pk_fma_f32 v[32:33], v[28:29], v[32:33], v[58:59]
	v_pk_fma_f32 v[54:55], v[30:31], v[54:55], v[60:61]
	v_and_b32_e32 v57, 0x7fffffff, v33
	v_and_b32_e32 v56, 0x7fffffff, v32
	v_pk_fma_f32 v[56:57], v[56:57], s[10:11], 1.0 op_sel_hi:[1,0,0]
	v_pk_mul_f32 v[64:65], v[32:33], v[32:33]
	v_rcp_f32_e32 v56, v56
	v_rcp_f32_e32 v57, v57
	v_pk_mul_f32 v[64:65], v[64:65], s[14:15] op_sel_hi:[1,0]
	v_cmp_gt_f32_e32 vcc, 0, v33
	v_exp_f32_e32 v64, v64
	v_pk_fma_f32 v[62:63], v[56:57], s[6:7], v[14:15] op_sel_hi:[1,0,0]
	v_exp_f32_e32 v65, v65
	v_pk_fma_f32 v[62:63], v[56:57], v[62:63], s[12:13] op_sel_hi:[1,1,0]
	v_pk_fma_f32 v[28:29], v[28:29], v[52:53], v[58:59]
	v_pk_fma_f32 v[62:63], v[56:57], v[62:63], s[8:9] op_sel_hi:[1,1,0]
	v_and_b32_e32 v53, 0x7fffffff, v29
	v_pk_fma_f32 v[62:63], v[56:57], v[62:63], s[16:17] op_sel_hi:[1,1,0]
	v_and_b32_e32 v52, 0x7fffffff, v28
	v_pk_mul_f32 v[56:57], v[56:57], v[62:63]
	v_pk_fma_f32 v[52:53], v[52:53], s[10:11], 1.0 op_sel_hi:[1,0,0]
	v_pk_mul_f32 v[56:57], v[64:65], v[56:57]
	v_and_b32_e32 v65, 0x7fffffff, v55
	v_and_b32_e32 v64, 0x7fffffff, v54
	v_pk_fma_f32 v[64:65], v[64:65], s[10:11], 1.0 op_sel_hi:[1,0,0]
	v_pk_mul_f32 v[62:63], v[32:33], v[56:57]
	v_rcp_f32_e32 v64, v64
	v_rcp_f32_e32 v65, v65
	v_pk_fma_f32 v[56:57], v[32:33], v[56:57], v[32:33] neg_lo:[1,0,0] neg_hi:[1,0,0]
	v_rcp_f32_e32 v52, v52
	v_cndmask_b32_e32 v33, v57, v63, vcc
	v_cmp_gt_f32_e32 vcc, 0, v32
	v_rcp_f32_e32 v53, v53
	v_pk_fma_f32 v[30:31], v[30:31], v[50:51], v[60:61]
	v_cndmask_b32_e32 v32, v56, v62, vcc
	v_pk_mul_f32 v[62:63], v[54:55], v[54:55]
	v_pk_fma_f32 v[56:57], v[64:65], s[6:7], v[14:15] op_sel_hi:[1,0,0]
	v_pk_mul_f32 v[62:63], v[62:63], s[14:15] op_sel_hi:[1,0]
	v_pk_fma_f32 v[56:57], v[64:65], v[56:57], s[12:13] op_sel_hi:[1,1,0]
	v_exp_f32_e32 v62, v62
	v_exp_f32_e32 v63, v63
	v_pk_fma_f32 v[56:57], v[64:65], v[56:57], s[8:9] op_sel_hi:[1,1,0]
	v_cmp_gt_f32_e32 vcc, 0, v55
	v_pk_fma_f32 v[56:57], v[64:65], v[56:57], s[16:17] op_sel_hi:[1,1,0]
	v_cvt_pk_f16_f32 v32, v32, v33
	v_pk_mul_f32 v[56:57], v[64:65], v[56:57]
	v_and_b32_e32 v51, 0x7fffffff, v31
	v_pk_mul_f32 v[56:57], v[62:63], v[56:57]
	v_and_b32_e32 v50, 0x7fffffff, v30
	v_pk_mul_f32 v[62:63], v[54:55], v[56:57]
	v_pk_fma_f32 v[56:57], v[54:55], v[56:57], v[54:55] neg_lo:[1,0,0] neg_hi:[1,0,0]
	v_pk_fma_f32 v[50:51], v[50:51], s[10:11], 1.0 op_sel_hi:[1,0,0]
	v_cndmask_b32_e32 v33, v57, v63, vcc
	v_cmp_gt_f32_e32 vcc, 0, v54
	v_rcp_f32_e32 v50, v50
	v_rcp_f32_e32 v51, v51
	v_cndmask_b32_e32 v54, v56, v62, vcc
	v_cvt_pk_f16_f32 v33, v54, v33
	v_pk_mul_f32 v[54:55], v[28:29], v[28:29]
	ds_write_b64 v13, v[32:33] offset:48
	v_pk_fma_f32 v[32:33], v[52:53], s[6:7], v[14:15] op_sel_hi:[1,0,0]
	v_pk_mul_f32 v[54:55], v[54:55], s[14:15] op_sel_hi:[1,0]
	v_pk_fma_f32 v[32:33], v[52:53], v[32:33], s[12:13] op_sel_hi:[1,1,0]
	v_exp_f32_e32 v54, v54
	v_exp_f32_e32 v55, v55
	v_pk_fma_f32 v[32:33], v[52:53], v[32:33], s[8:9] op_sel_hi:[1,1,0]
	v_cmp_gt_f32_e32 vcc, 0, v29
	v_pk_fma_f32 v[32:33], v[52:53], v[32:33], s[16:17] op_sel_hi:[1,1,0]
	v_pk_add_f32 v[6:7], v[6:7], v[16:17] op_sel_hi:[1,0] neg_lo:[0,1] neg_hi:[0,1]
	v_pk_mul_f32 v[32:33], v[52:53], v[32:33]
	v_pk_add_f32 v[4:5], v[4:5], v[10:11] op_sel_hi:[1,0] neg_lo:[0,1] neg_hi:[0,1]
	v_pk_mul_f32 v[32:33], v[54:55], v[32:33]
	v_pk_mul_f32 v[4:5], v[4:5], v[12:13] op_sel_hi:[1,0]
	v_pk_mul_f32 v[52:53], v[28:29], v[32:33]
	v_pk_fma_f32 v[32:33], v[28:29], v[32:33], v[28:29] neg_lo:[1,0,0] neg_hi:[1,0,0]
	v_pk_add_f32 v[2:3], v[2:3], v[10:11] op_sel_hi:[1,0] neg_lo:[0,1] neg_hi:[0,1]
	v_cndmask_b32_e32 v29, v33, v53, vcc
	v_cmp_gt_f32_e32 vcc, 0, v28
	v_pk_mul_f32 v[2:3], v[2:3], v[12:13] op_sel_hi:[1,0]
	s_nop 0
	v_cndmask_b32_e32 v28, v32, v52, vcc
	v_pk_mul_f32 v[52:53], v[30:31], v[30:31]
	v_pk_fma_f32 v[32:33], v[50:51], s[6:7], v[14:15] op_sel_hi:[1,0,0]
	v_pk_mul_f32 v[52:53], v[52:53], s[14:15] op_sel_hi:[1,0]
	v_pk_fma_f32 v[32:33], v[50:51], v[32:33], s[12:13] op_sel_hi:[1,1,0]
	v_exp_f32_e32 v52, v52
	v_exp_f32_e32 v53, v53
	v_pk_fma_f32 v[32:33], v[50:51], v[32:33], s[8:9] op_sel_hi:[1,1,0]
	v_cmp_gt_f32_e32 vcc, 0, v31
	v_pk_fma_f32 v[32:33], v[50:51], v[32:33], s[16:17] op_sel_hi:[1,1,0]
	v_cvt_pk_f16_f32 v28, v28, v29
	v_pk_mul_f32 v[32:33], v[50:51], v[32:33]
	s_nop 0
	v_pk_mul_f32 v[32:33], v[52:53], v[32:33]
	s_nop 0
	v_pk_mul_f32 v[50:51], v[30:31], v[32:33]
	v_pk_fma_f32 v[32:33], v[30:31], v[32:33], v[30:31] neg_lo:[1,0,0] neg_hi:[1,0,0]
	s_nop 0
	v_cndmask_b32_e32 v29, v33, v51, vcc
	v_cmp_gt_f32_e32 vcc, 0, v30
	s_nop 1
	v_cndmask_b32_e32 v30, v32, v50, vcc
	v_cvt_pk_f16_f32 v29, v30, v29
	ds_write_b64 v13, v[28:29] offset:33328
	v_or_b32_e32 v28, 0x80, v23
	v_add_u32_e32 v29, s7, v28
	v_add_u32_e32 v32, s11, v28
	ds_read_b128 v[28:31], v29
	ds_read_b128 v[50:53], v32
	v_pk_add_f32 v[32:33], v[48:49], v[16:17] op_sel_hi:[1,0] neg_lo:[0,1] neg_hi:[0,1]
	s_waitcnt lgkmcnt(0)
	v_pk_fma_f32 v[46:47], v[30:31], v[46:47], v[52:53]
	v_pk_mul_f32 v[32:33], v[32:33], v[22:23] op_sel_hi:[1,0]
	v_pk_fma_f32 v[30:31], v[30:31], v[42:43], v[52:53]
	v_pk_fma_f32 v[32:33], v[28:29], v[32:33], v[50:51]
	v_pk_fma_f32 v[28:29], v[28:29], v[44:45], v[50:51]
	v_and_b32_e32 v49, 0x7fffffff, v33
	v_and_b32_e32 v48, 0x7fffffff, v32
	v_pk_fma_f32 v[48:49], v[48:49], s[10:11], 1.0 op_sel_hi:[1,0,0]
	v_pk_mul_f32 v[56:57], v[32:33], v[32:33]
	v_rcp_f32_e32 v48, v48
	v_rcp_f32_e32 v49, v49
	v_pk_mul_f32 v[56:57], v[56:57], s[14:15] op_sel_hi:[1,0]
	v_cmp_gt_f32_e32 vcc, 0, v33
	v_exp_f32_e32 v56, v56
	v_pk_fma_f32 v[54:55], v[48:49], s[6:7], v[14:15] op_sel_hi:[1,0,0]
	v_exp_f32_e32 v57, v57
	v_pk_fma_f32 v[54:55], v[48:49], v[54:55], s[12:13] op_sel_hi:[1,1,0]
	v_and_b32_e32 v45, 0x7fffffff, v29
	v_pk_fma_f32 v[54:55], v[48:49], v[54:55], s[8:9] op_sel_hi:[1,1,0]
	v_and_b32_e32 v44, 0x7fffffff, v28
	v_pk_fma_f32 v[54:55], v[48:49], v[54:55], s[16:17] op_sel_hi:[1,1,0]
	v_pk_fma_f32 v[44:45], v[44:45], s[10:11], 1.0 op_sel_hi:[1,0,0]
	v_pk_mul_f32 v[48:49], v[48:49], v[54:55]
	v_rcp_f32_e32 v44, v44
	v_pk_mul_f32 v[48:49], v[56:57], v[48:49]
	v_and_b32_e32 v57, 0x7fffffff, v47
	v_and_b32_e32 v56, 0x7fffffff, v46
	v_pk_fma_f32 v[56:57], v[56:57], s[10:11], 1.0 op_sel_hi:[1,0,0]
	v_pk_mul_f32 v[54:55], v[32:33], v[48:49]
	v_rcp_f32_e32 v56, v56
	v_rcp_f32_e32 v57, v57
	v_pk_fma_f32 v[48:49], v[32:33], v[48:49], v[32:33] neg_lo:[1,0,0] neg_hi:[1,0,0]
	v_rcp_f32_e32 v45, v45
	v_cndmask_b32_e32 v33, v49, v55, vcc
	v_cmp_gt_f32_e32 vcc, 0, v32
	v_and_b32_e32 v43, 0x7fffffff, v31
	v_and_b32_e32 v42, 0x7fffffff, v30
	v_cndmask_b32_e32 v32, v48, v54, vcc
	v_pk_mul_f32 v[54:55], v[46:47], v[46:47]
	v_pk_fma_f32 v[48:49], v[56:57], s[6:7], v[14:15] op_sel_hi:[1,0,0]
	v_pk_mul_f32 v[54:55], v[54:55], s[14:15] op_sel_hi:[1,0]
	v_pk_fma_f32 v[48:49], v[56:57], v[48:49], s[12:13] op_sel_hi:[1,1,0]
	v_exp_f32_e32 v54, v54
	v_exp_f32_e32 v55, v55
	v_pk_fma_f32 v[48:49], v[56:57], v[48:49], s[8:9] op_sel_hi:[1,1,0]
	v_cmp_gt_f32_e32 vcc, 0, v47
	v_pk_fma_f32 v[48:49], v[56:57], v[48:49], s[16:17] op_sel_hi:[1,1,0]
	v_cvt_pk_f16_f32 v32, v32, v33
	v_pk_mul_f32 v[48:49], v[56:57], v[48:49]
	v_pk_fma_f32 v[42:43], v[42:43], s[10:11], 1.0 op_sel_hi:[1,0,0]
	v_pk_mul_f32 v[48:49], v[54:55], v[48:49]
	v_rcp_f32_e32 v42, v42
	v_pk_mul_f32 v[54:55], v[46:47], v[48:49]
	v_pk_fma_f32 v[48:49], v[46:47], v[48:49], v[46:47] neg_lo:[1,0,0] neg_hi:[1,0,0]
	v_rcp_f32_e32 v43, v43
	v_cndmask_b32_e32 v33, v49, v55, vcc
	v_cmp_gt_f32_e32 vcc, 0, v46
	s_nop 1
	v_cndmask_b32_e32 v46, v48, v54, vcc
	v_cvt_pk_f16_f32 v33, v46, v33
	v_pk_mul_f32 v[46:47], v[28:29], v[28:29]
	ds_write_b64 v13, v[32:33] offset:64
	v_pk_fma_f32 v[32:33], v[44:45], s[6:7], v[14:15] op_sel_hi:[1,0,0]
	v_pk_mul_f32 v[46:47], v[46:47], s[14:15] op_sel_hi:[1,0]
	v_pk_fma_f32 v[32:33], v[44:45], v[32:33], s[12:13] op_sel_hi:[1,1,0]
	v_exp_f32_e32 v46, v46
	v_exp_f32_e32 v47, v47
	v_pk_fma_f32 v[32:33], v[44:45], v[32:33], s[8:9] op_sel_hi:[1,1,0]
	v_cmp_gt_f32_e32 vcc, 0, v29
	v_pk_fma_f32 v[32:33], v[44:45], v[32:33], s[16:17] op_sel_hi:[1,1,0]
	s_nop 0
	v_pk_mul_f32 v[32:33], v[44:45], v[32:33]
	s_nop 0
	v_pk_mul_f32 v[32:33], v[46:47], v[32:33]
	s_nop 0
	v_pk_mul_f32 v[44:45], v[28:29], v[32:33]
	v_pk_fma_f32 v[32:33], v[28:29], v[32:33], v[28:29] neg_lo:[1,0,0] neg_hi:[1,0,0]
	s_nop 0
	v_cndmask_b32_e32 v29, v33, v45, vcc
	v_cmp_gt_f32_e32 vcc, 0, v28
	s_nop 1
	v_cndmask_b32_e32 v28, v32, v44, vcc
	v_pk_mul_f32 v[44:45], v[30:31], v[30:31]
	v_pk_fma_f32 v[32:33], v[42:43], s[6:7], v[14:15] op_sel_hi:[1,0,0]
	v_pk_mul_f32 v[44:45], v[44:45], s[14:15] op_sel_hi:[1,0]
	v_pk_fma_f32 v[32:33], v[42:43], v[32:33], s[12:13] op_sel_hi:[1,1,0]
	v_exp_f32_e32 v44, v44
	v_exp_f32_e32 v45, v45
	v_pk_fma_f32 v[32:33], v[42:43], v[32:33], s[8:9] op_sel_hi:[1,1,0]
	v_cmp_gt_f32_e32 vcc, 0, v31
	v_pk_fma_f32 v[32:33], v[42:43], v[32:33], s[16:17] op_sel_hi:[1,1,0]
	v_cvt_pk_f16_f32 v28, v28, v29
	v_pk_mul_f32 v[32:33], v[42:43], v[32:33]
	s_nop 0
	v_pk_mul_f32 v[32:33], v[44:45], v[32:33]
	s_nop 0
	v_pk_mul_f32 v[42:43], v[30:31], v[32:33]
	v_pk_fma_f32 v[32:33], v[30:31], v[32:33], v[30:31] neg_lo:[1,0,0] neg_hi:[1,0,0]
	s_nop 0
	v_cndmask_b32_e32 v29, v33, v43, vcc
	v_cmp_gt_f32_e32 vcc, 0, v30
	s_nop 1
	v_cndmask_b32_e32 v30, v32, v42, vcc
	v_cvt_pk_f16_f32 v29, v30, v29
	ds_write_b64 v13, v[28:29] offset:33344
	v_or_b32_e32 v28, 0xa0, v23
	v_add_u32_e32 v29, s7, v28
	v_add_u32_e32 v32, s11, v28
	ds_read_b128 v[28:31], v29
	ds_read_b128 v[42:45], v32
	v_pk_add_f32 v[32:33], v[40:41], v[16:17] op_sel_hi:[1,0] neg_lo:[0,1] neg_hi:[0,1]
	s_waitcnt lgkmcnt(0)
	v_pk_fma_f32 v[38:39], v[30:31], v[38:39], v[44:45]
	v_pk_mul_f32 v[32:33], v[32:33], v[22:23] op_sel_hi:[1,0]
	v_pk_fma_f32 v[30:31], v[30:31], v[34:35], v[44:45]
	v_pk_fma_f32 v[32:33], v[28:29], v[32:33], v[42:43]
	v_pk_fma_f32 v[28:29], v[28:29], v[36:37], v[42:43]
	v_and_b32_e32 v41, 0x7fffffff, v33
	v_and_b32_e32 v40, 0x7fffffff, v32
	v_pk_fma_f32 v[40:41], v[40:41], s[10:11], 1.0 op_sel_hi:[1,0,0]
	v_pk_mul_f32 v[48:49], v[32:33], v[32:33]
	v_rcp_f32_e32 v40, v40
	v_rcp_f32_e32 v41, v41
	v_pk_mul_f32 v[48:49], v[48:49], s[14:15] op_sel_hi:[1,0]
	v_cmp_gt_f32_e32 vcc, 0, v33
	v_exp_f32_e32 v48, v48
	v_pk_fma_f32 v[46:47], v[40:41], s[6:7], v[14:15] op_sel_hi:[1,0,0]
	v_exp_f32_e32 v49, v49
	v_pk_fma_f32 v[46:47], v[40:41], v[46:47], s[12:13] op_sel_hi:[1,1,0]
	v_and_b32_e32 v37, 0x7fffffff, v29
	v_pk_fma_f32 v[46:47], v[40:41], v[46:47], s[8:9] op_sel_hi:[1,1,0]
	v_and_b32_e32 v36, 0x7fffffff, v28
	v_pk_fma_f32 v[46:47], v[40:41], v[46:47], s[16:17] op_sel_hi:[1,1,0]
	v_pk_fma_f32 v[36:37], v[36:37], s[10:11], 1.0 op_sel_hi:[1,0,0]
	v_pk_mul_f32 v[40:41], v[40:41], v[46:47]
	v_rcp_f32_e32 v36, v36
	v_pk_mul_f32 v[40:41], v[48:49], v[40:41]
	v_and_b32_e32 v49, 0x7fffffff, v39
	v_and_b32_e32 v48, 0x7fffffff, v38
	v_pk_fma_f32 v[48:49], v[48:49], s[10:11], 1.0 op_sel_hi:[1,0,0]
	v_pk_mul_f32 v[46:47], v[32:33], v[40:41]
	v_rcp_f32_e32 v48, v48
	v_rcp_f32_e32 v49, v49
	v_pk_fma_f32 v[40:41], v[32:33], v[40:41], v[32:33] neg_lo:[1,0,0] neg_hi:[1,0,0]
	v_rcp_f32_e32 v37, v37
	v_cndmask_b32_e32 v33, v41, v47, vcc
	v_cmp_gt_f32_e32 vcc, 0, v32
	v_and_b32_e32 v35, 0x7fffffff, v31
	v_and_b32_e32 v34, 0x7fffffff, v30
	v_cndmask_b32_e32 v32, v40, v46, vcc
	v_pk_mul_f32 v[46:47], v[38:39], v[38:39]
	v_pk_fma_f32 v[40:41], v[48:49], s[6:7], v[14:15] op_sel_hi:[1,0,0]
	v_pk_mul_f32 v[46:47], v[46:47], s[14:15] op_sel_hi:[1,0]
	v_pk_fma_f32 v[40:41], v[48:49], v[40:41], s[12:13] op_sel_hi:[1,1,0]
	v_exp_f32_e32 v46, v46
	v_exp_f32_e32 v47, v47
	v_pk_fma_f32 v[40:41], v[48:49], v[40:41], s[8:9] op_sel_hi:[1,1,0]
	v_cmp_gt_f32_e32 vcc, 0, v39
	v_pk_fma_f32 v[40:41], v[48:49], v[40:41], s[16:17] op_sel_hi:[1,1,0]
	v_cvt_pk_f16_f32 v32, v32, v33
	v_pk_mul_f32 v[40:41], v[48:49], v[40:41]
	v_pk_fma_f32 v[34:35], v[34:35], s[10:11], 1.0 op_sel_hi:[1,0,0]
	v_pk_mul_f32 v[40:41], v[46:47], v[40:41]
	v_rcp_f32_e32 v34, v34
	v_pk_mul_f32 v[46:47], v[38:39], v[40:41]
	v_pk_fma_f32 v[40:41], v[38:39], v[40:41], v[38:39] neg_lo:[1,0,0] neg_hi:[1,0,0]
	v_rcp_f32_e32 v35, v35
	v_cndmask_b32_e32 v33, v41, v47, vcc
	v_cmp_gt_f32_e32 vcc, 0, v38
	s_nop 1
	v_cndmask_b32_e32 v38, v40, v46, vcc
	v_cvt_pk_f16_f32 v33, v38, v33
	v_pk_mul_f32 v[38:39], v[28:29], v[28:29]
	ds_write_b64 v13, v[32:33] offset:80
	v_pk_fma_f32 v[32:33], v[36:37], s[6:7], v[14:15] op_sel_hi:[1,0,0]
	v_pk_mul_f32 v[38:39], v[38:39], s[14:15] op_sel_hi:[1,0]
	v_pk_fma_f32 v[32:33], v[36:37], v[32:33], s[12:13] op_sel_hi:[1,1,0]
	v_exp_f32_e32 v38, v38
	v_exp_f32_e32 v39, v39
	v_pk_fma_f32 v[32:33], v[36:37], v[32:33], s[8:9] op_sel_hi:[1,1,0]
	v_cmp_gt_f32_e32 vcc, 0, v29
	v_pk_fma_f32 v[32:33], v[36:37], v[32:33], s[16:17] op_sel_hi:[1,1,0]
	s_nop 0
	v_pk_mul_f32 v[32:33], v[36:37], v[32:33]
	s_nop 0
	v_pk_mul_f32 v[32:33], v[38:39], v[32:33]
	s_nop 0
	v_pk_mul_f32 v[36:37], v[28:29], v[32:33]
	v_pk_fma_f32 v[32:33], v[28:29], v[32:33], v[28:29] neg_lo:[1,0,0] neg_hi:[1,0,0]
	s_nop 0
	v_cndmask_b32_e32 v29, v33, v37, vcc
	v_cmp_gt_f32_e32 vcc, 0, v28
	s_nop 1
	v_cndmask_b32_e32 v28, v32, v36, vcc
	v_pk_mul_f32 v[36:37], v[30:31], v[30:31]
	v_pk_fma_f32 v[32:33], v[34:35], s[6:7], v[14:15] op_sel_hi:[1,0,0]
	v_pk_mul_f32 v[36:37], v[36:37], s[14:15] op_sel_hi:[1,0]
	v_pk_fma_f32 v[32:33], v[34:35], v[32:33], s[12:13] op_sel_hi:[1,1,0]
	v_exp_f32_e32 v36, v36
	v_exp_f32_e32 v37, v37
	v_pk_fma_f32 v[32:33], v[34:35], v[32:33], s[8:9] op_sel_hi:[1,1,0]
	v_cmp_gt_f32_e32 vcc, 0, v31
	v_pk_fma_f32 v[32:33], v[34:35], v[32:33], s[16:17] op_sel_hi:[1,1,0]
	v_cvt_pk_f16_f32 v28, v28, v29
	v_pk_mul_f32 v[32:33], v[34:35], v[32:33]
	s_nop 0
	v_pk_mul_f32 v[32:33], v[36:37], v[32:33]
	s_nop 0
	v_pk_mul_f32 v[34:35], v[30:31], v[32:33]
	v_pk_fma_f32 v[32:33], v[30:31], v[32:33], v[30:31] neg_lo:[1,0,0] neg_hi:[1,0,0]
	s_nop 0
	v_cndmask_b32_e32 v29, v33, v35, vcc
	v_cmp_gt_f32_e32 vcc, 0, v30
	s_nop 1
	v_cndmask_b32_e32 v30, v32, v34, vcc
	v_cvt_pk_f16_f32 v29, v30, v29
	ds_write_b64 v13, v[28:29] offset:33360
	v_or_b32_e32 v28, 0xc0, v23
	v_add_u32_e32 v29, s7, v28
	v_add_u32_e32 v32, s11, v28
	ds_read_b128 v[28:31], v29
	ds_read_b128 v[32:35], v32
	s_waitcnt lgkmcnt(0)
	v_pk_fma_f32 v[26:27], v[28:29], v[26:27], v[32:33]
	s_nop 0
	v_and_b32_e32 v37, 0x7fffffff, v27
	v_and_b32_e32 v36, 0x7fffffff, v26
	v_pk_fma_f32 v[36:37], v[36:37], s[10:11], 1.0 op_sel_hi:[1,0,0]
	v_pk_mul_f32 v[40:41], v[26:27], v[26:27]
	v_rcp_f32_e32 v36, v36
	v_rcp_f32_e32 v37, v37
	v_pk_mul_f32 v[40:41], v[40:41], s[14:15] op_sel_hi:[1,0]
	v_pk_fma_f32 v[24:25], v[30:31], v[24:25], v[34:35]
	v_exp_f32_e32 v40, v40
	v_pk_fma_f32 v[38:39], v[36:37], s[6:7], v[14:15] op_sel_hi:[1,0,0]
	v_exp_f32_e32 v41, v41
	v_pk_fma_f32 v[38:39], v[36:37], v[38:39], s[12:13] op_sel_hi:[1,1,0]
	v_cmp_gt_f32_e32 vcc, 0, v27
	v_pk_fma_f32 v[38:39], v[36:37], v[38:39], s[8:9] op_sel_hi:[1,1,0]
	v_pk_fma_f32 v[20:21], v[28:29], v[20:21], v[32:33]
	v_pk_fma_f32 v[38:39], v[36:37], v[38:39], s[16:17] op_sel_hi:[1,1,0]
	v_and_b32_e32 v29, 0x7fffffff, v21
	v_pk_mul_f32 v[36:37], v[36:37], v[38:39]
	v_and_b32_e32 v28, 0x7fffffff, v20
	v_pk_mul_f32 v[36:37], v[40:41], v[36:37]
	v_and_b32_e32 v41, 0x7fffffff, v25
	v_and_b32_e32 v40, 0x7fffffff, v24
	v_pk_fma_f32 v[40:41], v[40:41], s[10:11], 1.0 op_sel_hi:[1,0,0]
	v_pk_mul_f32 v[38:39], v[26:27], v[36:37]
	v_rcp_f32_e32 v40, v40
	v_rcp_f32_e32 v41, v41
	v_pk_fma_f32 v[36:37], v[26:27], v[36:37], v[26:27] neg_lo:[1,0,0] neg_hi:[1,0,0]
	v_pk_fma_f32 v[28:29], v[28:29], s[10:11], 1.0 op_sel_hi:[1,0,0]
	v_cndmask_b32_e32 v27, v37, v39, vcc
	v_cmp_gt_f32_e32 vcc, 0, v26
	v_rcp_f32_e32 v28, v28
	v_rcp_f32_e32 v29, v29
	v_cndmask_b32_e32 v26, v36, v38, vcc
	v_pk_mul_f32 v[38:39], v[24:25], v[24:25]
	v_pk_fma_f32 v[36:37], v[40:41], s[6:7], v[14:15] op_sel_hi:[1,0,0]
	v_pk_mul_f32 v[38:39], v[38:39], s[14:15] op_sel_hi:[1,0]
	v_pk_fma_f32 v[36:37], v[40:41], v[36:37], s[12:13] op_sel_hi:[1,1,0]
	v_exp_f32_e32 v38, v38
	v_exp_f32_e32 v39, v39
	v_pk_fma_f32 v[36:37], v[40:41], v[36:37], s[8:9] op_sel_hi:[1,1,0]
	v_cmp_gt_f32_e32 vcc, 0, v25
	v_pk_fma_f32 v[36:37], v[40:41], v[36:37], s[16:17] op_sel_hi:[1,1,0]
	v_cvt_pk_f16_f32 v26, v26, v27
	v_pk_mul_f32 v[36:37], v[40:41], v[36:37]
	v_pk_fma_f32 v[18:19], v[30:31], v[18:19], v[34:35]
	v_pk_mul_f32 v[36:37], v[38:39], v[36:37]
	s_nop 0
	v_pk_mul_f32 v[38:39], v[24:25], v[36:37]
	v_pk_fma_f32 v[36:37], v[24:25], v[36:37], v[24:25] neg_lo:[1,0,0] neg_hi:[1,0,0]
	s_nop 0
	v_cndmask_b32_e32 v25, v37, v39, vcc
	v_cmp_gt_f32_e32 vcc, 0, v24
	s_nop 1
	v_cndmask_b32_e32 v24, v36, v38, vcc
	v_cvt_pk_f16_f32 v27, v24, v25
	ds_write_b64 v13, v[26:27] offset:96
	v_pk_fma_f32 v[24:25], v[28:29], s[6:7], v[14:15] op_sel_hi:[1,0,0]
	v_pk_mul_f32 v[26:27], v[20:21], v[20:21]
	v_pk_fma_f32 v[24:25], v[28:29], v[24:25], s[12:13] op_sel_hi:[1,1,0]
	v_pk_mul_f32 v[26:27], v[26:27], s[14:15] op_sel_hi:[1,0]
	v_pk_fma_f32 v[24:25], v[28:29], v[24:25], s[8:9] op_sel_hi:[1,1,0]
	v_exp_f32_e32 v26, v26
	v_exp_f32_e32 v27, v27
	v_pk_fma_f32 v[24:25], v[28:29], v[24:25], s[16:17] op_sel_hi:[1,1,0]
	v_cmp_gt_f32_e32 vcc, 0, v21
	v_pk_mul_f32 v[24:25], v[28:29], v[24:25]
	v_and_b32_e32 v29, 0x7fffffff, v19
	v_and_b32_e32 v28, 0x7fffffff, v18
	v_pk_fma_f32 v[28:29], v[28:29], s[10:11], 1.0 op_sel_hi:[1,0,0]
	v_pk_mul_f32 v[24:25], v[26:27], v[24:25]
	v_rcp_f32_e32 v28, v28
	v_rcp_f32_e32 v29, v29
	v_pk_mul_f32 v[26:27], v[20:21], v[24:25]
	v_pk_fma_f32 v[24:25], v[20:21], v[24:25], v[20:21] neg_lo:[1,0,0] neg_hi:[1,0,0]
	s_nop 0
	v_cndmask_b32_e32 v21, v25, v27, vcc
	v_cmp_gt_f32_e32 vcc, 0, v20
	s_nop 1
	v_cndmask_b32_e32 v20, v24, v26, vcc
	v_pk_mul_f32 v[26:27], v[18:19], v[18:19]
	v_pk_fma_f32 v[24:25], v[28:29], s[6:7], v[14:15] op_sel_hi:[1,0,0]
	v_pk_mul_f32 v[26:27], v[26:27], s[14:15] op_sel_hi:[1,0]
	v_pk_fma_f32 v[24:25], v[28:29], v[24:25], s[12:13] op_sel_hi:[1,1,0]
	v_exp_f32_e32 v26, v26
	v_exp_f32_e32 v27, v27
	v_pk_fma_f32 v[24:25], v[28:29], v[24:25], s[8:9] op_sel_hi:[1,1,0]
	v_cmp_gt_f32_e32 vcc, 0, v19
	v_pk_fma_f32 v[24:25], v[28:29], v[24:25], s[16:17] op_sel_hi:[1,1,0]
	v_cvt_pk_f16_f32 v20, v20, v21
	v_pk_mul_f32 v[24:25], v[28:29], v[24:25]
	s_nop 0
	v_pk_mul_f32 v[24:25], v[26:27], v[24:25]
	s_nop 0
	v_pk_mul_f32 v[26:27], v[18:19], v[24:25]
	v_pk_fma_f32 v[24:25], v[18:19], v[24:25], v[18:19] neg_lo:[1,0,0] neg_hi:[1,0,0]
	s_nop 0
	v_cndmask_b32_e32 v19, v25, v27, vcc
	v_cmp_gt_f32_e32 vcc, 0, v18
	s_nop 1
	v_cndmask_b32_e32 v18, v24, v26, vcc
	v_cvt_pk_f16_f32 v21, v18, v19
	v_or_b32_e32 v18, 0xe0, v23
	ds_write_b64 v13, v[20:21] offset:33376
	v_add_u32_e32 v19, s7, v18
	v_add_u32_e32 v23, s11, v18
	ds_read_b128 v[18:21], v19
	ds_read_b128 v[24:27], v23
	v_pk_mul_f32 v[8:9], v[8:9], v[22:23] op_sel_hi:[1,0]
	v_pk_mul_f32 v[6:7], v[6:7], v[22:23] op_sel_hi:[1,0]
	s_waitcnt lgkmcnt(0)
	v_pk_fma_f32 v[8:9], v[18:19], v[8:9], v[24:25]
	s_nop 0
	v_and_b32_e32 v29, 0x7fffffff, v9
	v_and_b32_e32 v28, 0x7fffffff, v8
	v_pk_fma_f32 v[28:29], v[28:29], s[10:11], 1.0 op_sel_hi:[1,0,0]
	v_pk_mul_f32 v[32:33], v[8:9], v[8:9]
	v_rcp_f32_e32 v28, v28
	v_rcp_f32_e32 v29, v29
	v_pk_mul_f32 v[32:33], v[32:33], s[14:15] op_sel_hi:[1,0]
	v_pk_fma_f32 v[6:7], v[20:21], v[6:7], v[26:27]
	v_exp_f32_e32 v32, v32
	v_pk_fma_f32 v[30:31], v[28:29], s[6:7], v[14:15] op_sel_hi:[1,0,0]
	v_exp_f32_e32 v33, v33
	v_pk_fma_f32 v[30:31], v[28:29], v[30:31], s[12:13] op_sel_hi:[1,1,0]
	v_and_b32_e32 v17, 0x7fffffff, v7
	v_pk_fma_f32 v[30:31], v[28:29], v[30:31], s[8:9] op_sel_hi:[1,1,0]
	v_and_b32_e32 v16, 0x7fffffff, v6
	v_pk_fma_f32 v[30:31], v[28:29], v[30:31], s[16:17] op_sel_hi:[1,1,0]
	v_pk_fma_f32 v[16:17], v[16:17], s[10:11], 1.0 op_sel_hi:[1,0,0]
	v_pk_mul_f32 v[28:29], v[28:29], v[30:31]
	v_rcp_f32_e32 v16, v16
	v_pk_mul_f32 v[28:29], v[32:33], v[28:29]
	v_rcp_f32_e32 v17, v17
	v_pk_mul_f32 v[30:31], v[8:9], v[28:29]
	v_pk_fma_f32 v[28:29], v[8:9], v[28:29], v[8:9] neg_lo:[1,0,0] neg_hi:[1,0,0]
	v_cmp_gt_f32_e32 vcc, 0, v9
	v_pk_fma_f32 v[22:23], v[16:17], s[6:7], v[14:15] op_sel_hi:[1,0,0]
	v_pk_fma_f32 v[4:5], v[18:19], v[4:5], v[24:25]
	v_cndmask_b32_e32 v9, v29, v31, vcc
	v_cmp_gt_f32_e32 vcc, 0, v8
	v_pk_fma_f32 v[22:23], v[16:17], v[22:23], s[12:13] op_sel_hi:[1,1,0]
	v_and_b32_e32 v19, 0x7fffffff, v5
	v_cndmask_b32_e32 v8, v28, v30, vcc
	v_pk_mul_f32 v[28:29], v[6:7], v[6:7]
	v_pk_fma_f32 v[22:23], v[16:17], v[22:23], s[8:9] op_sel_hi:[1,1,0]
	v_pk_mul_f32 v[28:29], v[28:29], s[14:15] op_sel_hi:[1,0]
	v_pk_fma_f32 v[22:23], v[16:17], v[22:23], s[16:17] op_sel_hi:[1,1,0]
	v_exp_f32_e32 v28, v28
	v_exp_f32_e32 v29, v29
	v_pk_mul_f32 v[16:17], v[16:17], v[22:23]
	v_and_b32_e32 v18, 0x7fffffff, v4
	v_cmp_gt_f32_e32 vcc, 0, v7
	v_pk_mul_f32 v[16:17], v[28:29], v[16:17]
	v_pk_fma_f32 v[18:19], v[18:19], s[10:11], 1.0 op_sel_hi:[1,0,0]
	v_pk_mul_f32 v[22:23], v[6:7], v[16:17]
	v_pk_fma_f32 v[16:17], v[6:7], v[16:17], v[6:7] neg_lo:[1,0,0] neg_hi:[1,0,0]
	v_rcp_f32_e32 v18, v18
	v_cndmask_b32_e32 v7, v17, v23, vcc
	v_rcp_f32_e32 v19, v19
	v_cmp_gt_f32_e32 vcc, 0, v6
	v_cvt_pk_f16_f32 v8, v8, v9
	v_pk_fma_f32 v[2:3], v[20:21], v[2:3], v[26:27]
	v_cndmask_b32_e32 v6, v16, v22, vcc
	v_cvt_pk_f16_f32 v9, v6, v7
	ds_write_b64 v13, v[8:9] offset:112
	v_pk_mul_f32 v[8:9], v[4:5], v[4:5]
	v_pk_fma_f32 v[6:7], v[18:19], s[6:7], v[14:15] op_sel_hi:[1,0,0]
	v_pk_mul_f32 v[8:9], v[8:9], s[14:15] op_sel_hi:[1,0]
	v_pk_fma_f32 v[6:7], v[18:19], v[6:7], s[12:13] op_sel_hi:[1,1,0]
	v_exp_f32_e32 v8, v8
	v_exp_f32_e32 v9, v9
	v_pk_fma_f32 v[6:7], v[18:19], v[6:7], s[8:9] op_sel_hi:[1,1,0]
	v_and_b32_e32 v11, 0x7fffffff, v3
	v_pk_fma_f32 v[6:7], v[18:19], v[6:7], s[16:17] op_sel_hi:[1,1,0]
	v_and_b32_e32 v10, 0x7fffffff, v2
	v_pk_mul_f32 v[6:7], v[18:19], v[6:7]
	v_pk_fma_f32 v[10:11], v[10:11], s[10:11], 1.0 op_sel_hi:[1,0,0]
	v_pk_mul_f32 v[6:7], v[8:9], v[6:7]
	v_rcp_f32_e32 v10, v10
	v_rcp_f32_e32 v11, v11
	v_pk_mul_f32 v[8:9], v[4:5], v[6:7]
	v_pk_fma_f32 v[6:7], v[4:5], v[6:7], v[4:5] neg_lo:[1,0,0] neg_hi:[1,0,0]
	v_cmp_gt_f32_e32 vcc, 0, v5
	s_nop 1
	v_cndmask_b32_e32 v5, v7, v9, vcc
	v_cmp_gt_f32_e32 vcc, 0, v4
	s_nop 1
	v_cndmask_b32_e32 v4, v6, v8, vcc
	v_pk_mul_f32 v[8:9], v[2:3], v[2:3]
	v_pk_fma_f32 v[6:7], v[10:11], s[6:7], v[14:15] op_sel_hi:[1,0,0]
	v_pk_mul_f32 v[8:9], v[8:9], s[14:15] op_sel_hi:[1,0]
	v_pk_fma_f32 v[6:7], v[10:11], v[6:7], s[12:13] op_sel_hi:[1,1,0]
	v_exp_f32_e32 v8, v8
	v_exp_f32_e32 v9, v9
	v_pk_fma_f32 v[6:7], v[10:11], v[6:7], s[8:9] op_sel_hi:[1,1,0]
	v_cmp_gt_f32_e32 vcc, 0, v3
	v_pk_fma_f32 v[6:7], v[10:11], v[6:7], s[16:17] op_sel_hi:[1,1,0]
	v_cvt_pk_f16_f32 v4, v4, v5
	v_pk_mul_f32 v[6:7], v[10:11], v[6:7]
	s_nop 0
	v_pk_mul_f32 v[6:7], v[8:9], v[6:7]
	s_nop 0
	v_pk_mul_f32 v[8:9], v[2:3], v[6:7]
	v_pk_fma_f32 v[6:7], v[2:3], v[6:7], v[2:3] neg_lo:[1,0,0] neg_hi:[1,0,0]
	s_nop 0
	v_cndmask_b32_e32 v3, v7, v9, vcc
	v_cmp_gt_f32_e32 vcc, 0, v2
	s_nop 1
	v_cndmask_b32_e32 v2, v6, v8, vcc
	v_cvt_pk_f16_f32 v5, v2, v3
	ds_write_b64 v13, v[4:5] offset:33392
	s_waitcnt lgkmcnt(0)
	s_barrier
	s_cmp_lt_u32 s18, 4
	s_cbranch_scc1 .Lmy_ffn_nostag3
	s_sleep 2
.Lmy_ffn_nostag3:
	ds_read_b128 v[2:5], v202
	ds_read_b128 v[38:41], v202 offset:32
	ds_read_b128 v[6:9], v202 offset:33280
	ds_read_b128 v[42:45], v202 offset:33312
	s_waitcnt vmcnt(7) lgkmcnt(3)
	v_mfma_f32_32x32x16_f16 v[18:33], v[126:129], v[2:5], 0
	ds_read_b128 v[46:49], v202 offset:64
	ds_read_b128 v[50:53], v202 offset:33344
	ds_read_b128 v[34:37], v204
	s_waitcnt lgkmcnt(4)
	v_mfma_f32_32x32x16_f16 v[2:17], v[126:129], v[6:9], 0
	s_waitcnt vmcnt(6)
	v_mfma_f32_32x32x16_f16 v[18:33], v[122:125], v[38:41], v[18:33]
	ds_read_b128 v[54:57], v202 offset:96
	ds_read_b128 v[58:61], v202 offset:33376
	ds_read_b128 v[38:41], v204 offset:1024
	s_waitcnt lgkmcnt(6)
	v_mfma_f32_32x32x16_f16 v[2:17], v[122:125], v[42:45], v[2:17]
	s_waitcnt vmcnt(5) lgkmcnt(5)
	v_mfma_f32_32x32x16_f16 v[18:33], v[118:121], v[46:49], v[18:33]
	ds_read_b128 v[62:65], v202 offset:128
	ds_read_b128 v[122:125], v202 offset:33408
	ds_read_b128 v[42:45], v204 offset:2048
	s_waitcnt lgkmcnt(7)
	v_mfma_f32_32x32x16_f16 v[2:17], v[118:121], v[50:53], v[2:17]
	s_waitcnt vmcnt(4) lgkmcnt(5)
	v_mfma_f32_32x32x16_f16 v[18:33], v[114:117], v[54:57], v[18:33]
	ds_read_b128 v[50:53], v202 offset:160
	ds_read_b128 v[118:121], v202 offset:33440
	ds_read_b128 v[46:49], v204 offset:3072
	s_waitcnt lgkmcnt(7)
	v_mfma_f32_32x32x16_f16 v[2:17], v[114:117], v[58:61], v[2:17]
	s_waitcnt vmcnt(3) lgkmcnt(5)
	v_mfma_f32_32x32x16_f16 v[18:33], v[110:113], v[62:65], v[18:33]
	ds_read_b128 v[58:61], v202 offset:192
	ds_read_b128 v[62:65], v202 offset:33472
	ds_read_b128 v[54:57], v204 offset:4096
	s_waitcnt lgkmcnt(7)
	v_mfma_f32_32x32x16_f16 v[2:17], v[110:113], v[122:125], v[2:17]
	s_waitcnt vmcnt(2) lgkmcnt(5)
	v_mfma_f32_32x32x16_f16 v[18:33], v[106:109], v[50:53], v[18:33]
	ds_read_b128 v[122:125], v202 offset:224
	ds_read_b128 v[126:129], v202 offset:33504
	ds_read_b128 v[50:53], v204 offset:5120
	s_waitcnt lgkmcnt(7)
	v_mfma_f32_32x32x16_f16 v[2:17], v[106:109], v[118:121], v[2:17]
	s_waitcnt vmcnt(1) lgkmcnt(5)
	v_mfma_f32_32x32x16_f16 v[18:33], v[102:105], v[58:61], v[18:33]
	ds_read_b128 v[114:117], v202 offset:256
	ds_read_b128 v[110:113], v202 offset:33536
	ds_read_b128 v[58:61], v204 offset:6144
	s_waitcnt lgkmcnt(7)
	v_mfma_f32_32x32x16_f16 v[2:17], v[102:105], v[62:65], v[2:17]
	s_waitcnt vmcnt(0) lgkmcnt(5)
	v_mfma_f32_32x32x16_f16 v[18:33], v[98:101], v[122:125], v[18:33]
	ds_read_b128 v[106:109], v202 offset:288
	ds_read_b128 v[102:105], v202 offset:33568
	ds_read_b128 v[62:65], v204 offset:7168
	s_waitcnt lgkmcnt(7)
	v_mfma_f32_32x32x16_f16 v[2:17], v[98:101], v[126:129], v[2:17]
	s_mov_b64 s[6:7], 0x4000
	v_lshl_add_u64 v[98:99], v[174:175], 0, s[6:7]
	s_mov_b64 s[6:7], 0x1000

	.amdhsa_kernel _Z10ffn_kernelPKfS0_PKDF16_S2_S0_S2_S0_S0_S0_S2_S0_Pf
		.amdhsa_group_segment_fixed_size 0
		.amdhsa_private_segment_fixed_size 0
		.amdhsa_kernarg_size 96
		.amdhsa_user_sgpr_count 2
		.amdhsa_user_sgpr_dispatch_ptr 0
		.amdhsa_user_sgpr_queue_ptr 0
		.amdhsa_user_sgpr_kernarg_segment_ptr 1
		.amdhsa_user_sgpr_dispatch_id 0
		.amdhsa_user_sgpr_kernarg_preload_length 0
		.amdhsa_user_sgpr_kernarg_preload_offset 0
		.amdhsa_user_sgpr_private_segment_size 0
		.amdhsa_uses_dynamic_stack 0
		.amdhsa_enable_private_segment 0
		.amdhsa_system_sgpr_workgroup_id_x 1
		.amdhsa_system_sgpr_workgroup_id_y 0
		.amdhsa_system_sgpr_workgroup_id_z 0
		.amdhsa_system_sgpr_workgroup_info 0
		.amdhsa_system_vgpr_workitem_id 0
		.amdhsa_next_free_vgpr 230
		.amdhsa_next_free_sgpr 19
		.amdhsa_accum_offset 232
		.amdhsa_reserve_vcc 1
		.amdhsa_float_round_mode_32 0
		.amdhsa_float_round_mode_16_64 0
		.amdhsa_float_denorm_mode_32 3
		.amdhsa_float_denorm_mode_16_64 3
		.amdhsa_dx10_clamp 1
		.amdhsa_ieee_mode 1
		.amdhsa_fp16_overflow 0
		.amdhsa_tg_split 0
		.amdhsa_exception_fp_ieee_invalid_op 0
		.amdhsa_exception_fp_denorm_src 0
		.amdhsa_exception_fp_ieee_div_zero 0
		.amdhsa_exception_fp_ieee_overflow 0
		.amdhsa_exception_fp_ieee_underflow 0
		.amdhsa_exception_fp_ieee_inexact 0
		.amdhsa_exception_int_div_zero 0
	.end_amdhsa_kernel

amdhsa.kernels:
  - .agpr_count:     0
    .args:
      - .actual_access:  read_only
        .address_space:  global
        .offset:         0
        .size:           8
        .value_kind:     global_buffer
      - .actual_access:  read_only
        .address_space:  global
        .offset:         8
        .size:           8
        .value_kind:     global_buffer
      - .actual_access:  read_only
        .address_space:  global
        .offset:         16
        .size:           8
        .value_kind:     global_buffer
      - .actual_access:  read_only
        .address_space:  global
        .offset:         24
        .size:           8
        .value_kind:     global_buffer
      - .actual_access:  read_only
        .address_space:  global
        .offset:         32
        .size:           8
        .value_kind:     global_buffer
      - .actual_access:  write_only
        .address_space:  global
        .offset:         40
        .size:           8
        .value_kind:     global_buffer
      - .actual_access:  write_only
        .address_space:  global
        .offset:         48
        .size:           8
        .value_kind:     global_buffer
      - .actual_access:  write_only
        .address_space:  global
        .offset:         56
        .size:           8
        .value_kind:     global_buffer
      - .actual_access:  write_only
        .address_space:  global
        .offset:         64
        .size:           8
        .value_kind:     global_buffer
    .group_segment_fixed_size: 0
    .kernarg_segment_align: 8
    .kernarg_segment_size: 72
    .language:       OpenCL C
    .language_version:
      - 2
      - 0
    .max_flat_workgroup_size: 256
    .name:           _Z11prep_kernelPKfS0_S0_S0_S0_PDF16_S1_S1_S1_
    .private_segment_fixed_size: 0
    .sgpr_count:     21
    .sgpr_spill_count: 0
    .symbol:         _Z11prep_kernelPKfS0_S0_S0_S0_PDF16_S1_S1_S1_.kd
    .uniform_work_group_size: 1
    .uses_dynamic_stack: false
    .vgpr_count:     18
    .vgpr_spill_count: 0
    .wavefront_size: 64
  - .agpr_count:     0
    .args:
      - .actual_access:  read_only
        .address_space:  global
        .offset:         0
        .size:           8
        .value_kind:     global_buffer
      - .actual_access:  read_only
        .address_space:  global
        .offset:         8
        .size:           8
        .value_kind:     global_buffer
      - .actual_access:  read_only
        .address_space:  global
        .offset:         16
        .size:           8
        .value_kind:     global_buffer
      - .actual_access:  read_only
        .address_space:  global
        .offset:         24
        .size:           8
        .value_kind:     global_buffer
      - .actual_access:  read_only
        .address_space:  global
        .offset:         32
        .size:           8
        .value_kind:     global_buffer
      - .actual_access:  write_only
        .address_space:  global
        .offset:         40
        .size:           8
        .value_kind:     global_buffer
      - .actual_access:  write_only
        .address_space:  global
        .offset:         48
        .size:           8
        .value_kind:     global_buffer
    .group_segment_fixed_size: 0
    .kernarg_segment_align: 8
    .kernarg_segment_size: 56
    .language:       OpenCL C
    .language_version:
      - 2
      - 0
    .max_flat_workgroup_size: 512
    .name:           _Z11proj_kernelPKfS0_PKDF16_S0_S0_PDF16_S3_
    .private_segment_fixed_size: 0
    .sgpr_count:     22
    .sgpr_spill_count: 0
    .symbol:         _Z11proj_kernelPKfS0_PKDF16_S0_S0_PDF16_S3_.kd
    .uniform_work_group_size: 1
    .uses_dynamic_stack: false
    .vgpr_count:     170
    .vgpr_spill_count: 0
    .wavefront_size: 64
  - .agpr_count:     0
    .args:
      - .address_space:  global
        .offset:         0
        .size:           8
        .value_kind:     global_buffer
      - .address_space:  global
        .offset:         8
        .size:           8
        .value_kind:     global_buffer
      - .actual_access:  write_only
        .address_space:  global
        .offset:         16
        .size:           8
        .value_kind:     global_buffer
    .group_segment_fixed_size: 0
    .kernarg_segment_align: 8
    .kernarg_segment_size: 24
    .language:       OpenCL C
    .language_version:
      - 2
      - 0
    .max_flat_workgroup_size: 512
    .name:           _Z11attn_kernelPKDF16_S0_PDF16_
    .private_segment_fixed_size: 0
    .sgpr_count:     56
    .sgpr_spill_count: 0
    .symbol:         _Z11attn_kernelPKDF16_S0_PDF16_.kd
    .uniform_work_group_size: 1
    .uses_dynamic_stack: false
    .vgpr_count:     192
    .vgpr_spill_count: 0
    .wavefront_size: 64
  - .agpr_count:     0
    .args:
      - .actual_access:  read_only
        .address_space:  global
        .offset:         0
        .size:           8
        .value_kind:     global_buffer
      - .actual_access:  read_only
        .address_space:  global
        .offset:         8
        .size:           8
        .value_kind:     global_buffer
      - .actual_access:  read_only
        .address_space:  global
        .offset:         16
        .size:           8
        .value_kind:     global_buffer
      - .actual_access:  read_only
        .address_space:  global
        .offset:         24
        .size:           8
        .value_kind:     global_buffer
      - .actual_access:  read_only
        .address_space:  global
        .offset:         32
        .size:           8
        .value_kind:     global_buffer
      - .address_space:  global
        .offset:         40
        .size:           8
        .value_kind:     global_buffer
      - .actual_access:  read_only
        .address_space:  global
        .offset:         48
        .size:           8
        .value_kind:     global_buffer
      - .actual_access:  read_only
        .address_space:  global
        .offset:         56
        .size:           8
        .value_kind:     global_buffer
      - .actual_access:  read_only
        .address_space:  global
        .offset:         64
        .size:           8
        .value_kind:     global_buffer
      - .address_space:  global
        .offset:         72
        .size:           8
        .value_kind:     global_buffer
      - .actual_access:  read_only
        .address_space:  global
        .offset:         80
        .size:           8
        .value_kind:     global_buffer
      - .actual_access:  write_only
        .address_space:  global
        .offset:         88
        .size:           8
        .value_kind:     global_buffer
    .group_segment_fixed_size: 0
    .kernarg_segment_align: 8
    .kernarg_segment_size: 96
    .language:       OpenCL C
    .language_version:
      - 2
      - 0
    .max_flat_workgroup_size: 512
    .name:           _Z10ffn_kernelPKfS0_PKDF16_S2_S0_S2_S0_S0_S0_S2_S0_Pf
    .private_segment_fixed_size: 0
    .sgpr_count:     25
    .sgpr_spill_count: 0
    .symbol:         _Z10ffn_kernelPKfS0_PKDF16_S2_S0_S2_S0_S0_S0_S2_S0_Pf.kd
    .uniform_work_group_size: 1
    .uses_dynamic_stack: false
    .vgpr_count:     230
    .vgpr_spill_count: 0
    .wavefront_size: 64
